# v73 + SGU swizzle term hoisted into a persistent VGPR (v232): 2 fewer VALU per normalise step
# speedup vs baseline: 1.0016x; 1.0016x over previous
.LBB0_488:
	s_or_b64 exec, exec, s[20:21]
	s_lshl_b64 s[4:5], s[52:53], 2
	s_add_u32 s13, s18, s4
	s_addc_u32 s21, s19, s5
	v_readlane_b32 s4, v255, 23
	v_readlane_b32 s5, v255, 24
	s_lshl_b64 s[4:5], s[4:5], 2
	s_add_u32 s16, s16, s4
	s_addc_u32 s17, s17, s5
	s_add_u32 s18, s10, 0x27c20000
	s_mul_i32 s4, s12, 0x4400
	s_addc_u32 s19, s11, 0
	s_add_i32 s20, s4, 0
	s_lshl_b64 s[4:5], s[6:7], 2
	v_lshlrev_b32_e32 v2, 3, v144
	s_add_u32 s4, s13, s4
	s_addc_u32 s5, s21, s5
	v_lshlrev_b32_e32 v6, 2, v2
	s_waitcnt lgkmcnt(0)
	s_barrier
	global_load_dwordx4 v[2:5], v6, s[4:5] offset:16
	s_nop 0
	global_load_dwordx4 v[6:9], v6, s[4:5]
	s_add_i32 s7, 0, 0x22000
	v_lshl_add_u32 v161, v0, 5, s7
	ds_read_b128 v[162:165], v161
	ds_read_b128 v[166:169], v161 offset:16
	v_and_b32_e32 v103, 63, v87
	v_and_b32_e32 v105, 31, v87
	v_or_b32_e32 v160, 8, v0
	s_waitcnt lgkmcnt(1)
	v_add_f32_e32 v161, v162, v163
	v_add_f32_e32 v162, v164, v165
	v_add_f32_e32 v161, v161, v162
	s_waitcnt lgkmcnt(0)
	v_add_f32_e32 v162, v166, v167
	v_add_f32_e32 v161, v161, v162
	v_add_f32_e32 v162, v168, v169
	v_add_f32_e32 v161, v162, v161
	v_fmamk_f32 v161, v161, 0x3b000000, v235
	v_rsq_f32_e32 v161, v161
	v_or_b32_e32 v159, 16, v0
	v_or_b32_e32 v150, 24, v0
	v_or_b32_e32 v149, 32, v0
	v_mul_f32_e32 v151, v161, v151
	v_or_b32_e32 v148, 40, v0
	v_or_b32_e32 v147, 48, v0
	v_or_b32_e32 v146, 56, v0
	v_or_b32_e32 v145, 64, v0
	v_or_b32_e32 v143, 0x48, v0
	v_or_b32_e32 v134, 0x50, v0
	v_or_b32_e32 v133, 0x58, v0
	v_or_b32_e32 v132, 0x60, v0
	v_or_b32_e32 v128, 0x68, v0
	v_or_b32_e32 v87, 0x70, v0
	v_or_b32_e32 v49, 0x78, v0
	v_mul_f32_e32 v152, v161, v152
	v_mul_f32_e32 v154, v161, v154
	v_mul_f32_e32 v153, v161, v153
	v_mul_f32_e32 v156, v161, v156
	v_mul_f32_e32 v155, v161, v155
	v_mul_f32_e32 v158, v161, v158
	v_mul_f32_e32 v157, v161, v157
	v_lshlrev_b32_e32 v161, 1, v0
	v_mul_u32_u24_e32 v0, 0x880, v144
	v_lshrrev_b32_e32 v144, 1, v144
	v_lshl_add_u32 v161, v144, 4, v161
	v_lshlrev_b32_e32 v232, 3, v144
	v_add3_u32 v144, s20, v161, v0
	s_ashr_i32 s13, s12, 31
	s_lshl_b64 s[4:5], s[12:13], 15
	v_lshrrev_b32_e32 v106, 5, v103
	s_add_u32 s4, s10, s4
	s_addc_u32 s5, s11, s5
	s_lshl_b32 s23, s12, 4
	s_waitcnt vmcnt(1)
	v_mul_f32_e32 v156, v2, v156
	s_waitcnt vmcnt(0)
	v_mul_f32_e32 v151, v7, v151
	v_mul_f32_e32 v154, v8, v154
	v_mul_f32_e32 v153, v9, v153
	v_cvt_pk_bf16_f32 v151, v151, v154
	ds_write_b16 v144, v151 offset:272
	ds_write_b16_d16_hi v144, v151 offset:544
	v_mul_f32_e32 v155, v3, v155
	v_mul_f32_e32 v158, v4, v158
	v_cvt_pk_bf16_f32 v151, v153, v156
	ds_write_b16 v144, v151 offset:816
	ds_write_b16_d16_hi v144, v151 offset:1088
	v_mul_f32_e32 v152, v6, v152
	v_mul_f32_e32 v157, v5, v157
	v_cvt_pk_bf16_f32 v151, v155, v158
	ds_write_b16 v144, v151 offset:1360
	ds_write_b16_d16_hi v144, v151 offset:1632
	v_cvt_pk_bf16_f32 v151, v152, v157
	ds_write_b16 v144, v151
	ds_write_b16_d16_hi v144, v151 offset:1904
	v_lshl_add_u32 v144, v160, 5, s7
	ds_read_b128 v[152:155], v144
	ds_read_b128 v[162:165], v144 offset:16
	s_waitcnt lgkmcnt(1)
	v_add_f32_e32 v144, v152, v153
	v_add_f32_e32 v151, v154, v155
	v_add_f32_e32 v144, v144, v151
	s_waitcnt lgkmcnt(0)
	v_add_f32_e32 v151, v162, v163
	v_add_f32_e32 v144, v144, v151
	v_add_f32_e32 v151, v164, v165
	v_add_f32_e32 v144, v151, v144
	v_fmamk_f32 v144, v144, 0x3b000000, v235
	v_rsq_f32_e32 v144, v144
	s_nop 0
	v_mul_f32_e32 v135, v144, v135
	v_mul_f32_e32 v136, v144, v136
	v_mul_f32_e32 v135, v7, v135
	v_mul_f32_e32 v138, v144, v138
	v_mul_f32_e32 v137, v144, v137
	v_mul_f32_e32 v140, v144, v140
	v_mul_f32_e32 v139, v144, v139
	v_mul_f32_e32 v142, v144, v142
	v_mul_f32_e32 v141, v144, v141
	v_xor_b32_e32 v144, v232, v160
	v_lshlrev_b32_e32 v144, 1, v144
	v_mul_f32_e32 v138, v8, v138
	v_add3_u32 v144, s20, v144, v0
	v_mul_f32_e32 v137, v9, v137
	v_mul_f32_e32 v140, v2, v140
	v_cvt_pk_bf16_f32 v135, v135, v138
	ds_write_b16 v144, v135 offset:272
	ds_write_b16_d16_hi v144, v135 offset:544
	v_mul_f32_e32 v139, v3, v139
	v_mul_f32_e32 v142, v4, v142
	v_cvt_pk_bf16_f32 v135, v137, v140
	ds_write_b16 v144, v135 offset:816
	ds_write_b16_d16_hi v144, v135 offset:1088
	v_mul_f32_e32 v136, v6, v136
	v_mul_f32_e32 v141, v5, v141
	v_cvt_pk_bf16_f32 v135, v139, v142
	ds_write_b16 v144, v135 offset:1360
	ds_write_b16_d16_hi v144, v135 offset:1632
	v_cvt_pk_bf16_f32 v135, v136, v141
	ds_write_b16 v144, v135
	ds_write_b16_d16_hi v144, v135 offset:1904
	v_lshl_add_u32 v135, v159, 5, s7
	ds_read_b128 v[136:139], v135
	ds_read_b128 v[152:155], v135 offset:16
	s_waitcnt lgkmcnt(1)
	v_add_f32_e32 v135, v136, v137
	v_add_f32_e32 v136, v138, v139
	v_add_f32_e32 v135, v135, v136
	s_waitcnt lgkmcnt(0)
	v_add_f32_e32 v136, v152, v153
	v_add_f32_e32 v135, v135, v136
	v_add_f32_e32 v136, v154, v155
	v_add_f32_e32 v135, v136, v135
	v_fmamk_f32 v135, v135, 0x3b000000, v235
	v_rsq_f32_e32 v135, v135
	s_nop 0
	v_mul_f32_e32 v123, v135, v123
	v_mul_f32_e32 v124, v135, v124
	v_mul_f32_e32 v123, v7, v123
	v_mul_f32_e32 v126, v135, v126
	v_mul_f32_e32 v125, v135, v125
	v_mul_f32_e32 v129, v135, v129
	v_mul_f32_e32 v127, v135, v127
	v_mul_f32_e32 v131, v135, v131
	v_mul_f32_e32 v130, v135, v130
	v_xor_b32_e32 v135, v232, v159
	v_lshlrev_b32_e32 v135, 1, v135
	v_mul_f32_e32 v126, v8, v126
	v_add3_u32 v135, s20, v135, v0
	v_mul_f32_e32 v125, v9, v125
	v_mul_f32_e32 v129, v2, v129
	v_cvt_pk_bf16_f32 v123, v123, v126
	ds_write_b16 v135, v123 offset:272
	ds_write_b16_d16_hi v135, v123 offset:544
	v_mul_f32_e32 v127, v3, v127
	v_mul_f32_e32 v131, v4, v131
	v_cvt_pk_bf16_f32 v123, v125, v129
	ds_write_b16 v135, v123 offset:816
	ds_write_b16_d16_hi v135, v123 offset:1088
	v_mul_f32_e32 v124, v6, v124
	v_mul_f32_e32 v130, v5, v130
	v_cvt_pk_bf16_f32 v123, v127, v131
	ds_write_b16 v135, v123 offset:1360
	ds_write_b16_d16_hi v135, v123 offset:1632
	v_cvt_pk_bf16_f32 v123, v124, v130
	ds_write_b16 v135, v123
	ds_write_b16_d16_hi v135, v123 offset:1904
	v_lshl_add_u32 v123, v150, 5, s7
	ds_read_b128 v[124:127], v123
	ds_read_b128 v[136:139], v123 offset:16
	s_waitcnt lgkmcnt(1)
	v_add_f32_e32 v123, v124, v125
	v_add_f32_e32 v124, v126, v127
	v_add_f32_e32 v123, v123, v124
	s_waitcnt lgkmcnt(0)
	v_add_f32_e32 v124, v136, v137
	v_add_f32_e32 v123, v123, v124
	v_add_f32_e32 v124, v138, v139
	v_add_f32_e32 v123, v124, v123
	v_fmamk_f32 v123, v123, 0x3b000000, v235
	v_rsq_f32_e32 v123, v123
	s_nop 0
	v_mul_f32_e32 v115, v123, v115
	v_mul_f32_e32 v116, v123, v116
	v_mul_f32_e32 v115, v7, v115
	v_mul_f32_e32 v118, v123, v118
	v_mul_f32_e32 v117, v123, v117
	v_mul_f32_e32 v120, v123, v120
	v_mul_f32_e32 v119, v123, v119
	v_mul_f32_e32 v122, v123, v122
	v_mul_f32_e32 v121, v123, v121
	v_xor_b32_e32 v123, v232, v150
	v_lshlrev_b32_e32 v123, 1, v123
	v_mul_f32_e32 v118, v8, v118
	v_add3_u32 v123, s20, v123, v0
	v_mul_f32_e32 v117, v9, v117
	v_mul_f32_e32 v120, v2, v120
	v_cvt_pk_bf16_f32 v115, v115, v118
	ds_write_b16 v123, v115 offset:272
	ds_write_b16_d16_hi v123, v115 offset:544
	v_mul_f32_e32 v119, v3, v119
	v_mul_f32_e32 v122, v4, v122
	v_cvt_pk_bf16_f32 v115, v117, v120
	ds_write_b16 v123, v115 offset:816
	ds_write_b16_d16_hi v123, v115 offset:1088
	v_mul_f32_e32 v116, v6, v116
	v_mul_f32_e32 v121, v5, v121
	v_cvt_pk_bf16_f32 v115, v119, v122
	ds_write_b16 v123, v115 offset:1360
	ds_write_b16_d16_hi v123, v115 offset:1632
	v_cvt_pk_bf16_f32 v115, v116, v121
	ds_write_b16 v123, v115
	ds_write_b16_d16_hi v123, v115 offset:1904
	v_lshl_add_u32 v115, v149, 5, s7
	ds_read_b128 v[116:119], v115
	ds_read_b128 v[120:123], v115 offset:16
	s_waitcnt lgkmcnt(1)
	v_add_f32_e32 v115, v116, v117
	v_add_f32_e32 v116, v118, v119
	v_add_f32_e32 v115, v115, v116
	s_waitcnt lgkmcnt(0)
	v_add_f32_e32 v116, v120, v121
	v_add_f32_e32 v115, v115, v116
	v_add_f32_e32 v116, v122, v123
	v_add_f32_e32 v115, v116, v115
	v_fmamk_f32 v115, v115, 0x3b000000, v235
	v_rsq_f32_e32 v115, v115
	s_nop 0
	v_mul_f32_e32 v107, v115, v107
	v_mul_f32_e32 v108, v115, v108
	v_mul_f32_e32 v107, v7, v107
	v_mul_f32_e32 v110, v115, v110
	v_mul_f32_e32 v109, v115, v109
	v_mul_f32_e32 v112, v115, v112
	v_mul_f32_e32 v111, v115, v111
	v_mul_f32_e32 v114, v115, v114
	v_mul_f32_e32 v113, v115, v113
	v_xor_b32_e32 v115, v232, v149
	v_lshlrev_b32_e32 v115, 1, v115
	v_mul_f32_e32 v110, v8, v110
	v_add3_u32 v115, s20, v115, v0
	v_mul_f32_e32 v109, v9, v109
	v_mul_f32_e32 v112, v2, v112
	v_cvt_pk_bf16_f32 v107, v107, v110
	ds_write_b16 v115, v107 offset:272
	ds_write_b16_d16_hi v115, v107 offset:544
	v_mul_f32_e32 v111, v3, v111
	v_mul_f32_e32 v114, v4, v114
	v_cvt_pk_bf16_f32 v107, v109, v112
	ds_write_b16 v115, v107 offset:816
	ds_write_b16_d16_hi v115, v107 offset:1088
	v_mul_f32_e32 v108, v6, v108
	v_mul_f32_e32 v113, v5, v113
	v_cvt_pk_bf16_f32 v107, v111, v114
	ds_write_b16 v115, v107 offset:1360
	ds_write_b16_d16_hi v115, v107 offset:1632
	v_cvt_pk_bf16_f32 v107, v108, v113
	ds_write_b16 v115, v107
	ds_write_b16_d16_hi v115, v107 offset:1904
	v_lshl_add_u32 v107, v148, 5, s7
	ds_read_b128 v[108:111], v107
	ds_read_b128 v[112:115], v107 offset:16
	s_waitcnt lgkmcnt(1)
	v_add_f32_e32 v107, v108, v109
	v_add_f32_e32 v108, v110, v111
	v_add_f32_e32 v107, v107, v108
	s_waitcnt lgkmcnt(0)
	v_add_f32_e32 v108, v112, v113
	v_add_f32_e32 v107, v107, v108
	v_add_f32_e32 v108, v114, v115
	v_add_f32_e32 v107, v108, v107
	v_fmamk_f32 v107, v107, 0x3b000000, v235
	v_rsq_f32_e32 v107, v107
	s_nop 0
	v_mul_f32_e32 v92, v107, v92
	v_mul_f32_e32 v93, v107, v93
	v_mul_f32_e32 v92, v7, v92
	v_mul_f32_e32 v95, v107, v95
	v_mul_f32_e32 v94, v107, v94
	v_mul_f32_e32 v97, v107, v97
	v_mul_f32_e32 v96, v107, v96
	v_mul_f32_e32 v99, v107, v99
	v_mul_f32_e32 v98, v107, v98
	v_xor_b32_e32 v107, v232, v148
	v_lshlrev_b32_e32 v107, 1, v107
	v_mul_f32_e32 v95, v8, v95
	v_add3_u32 v107, s20, v107, v0
	v_mul_f32_e32 v94, v9, v94
	v_mul_f32_e32 v97, v2, v97
	v_cvt_pk_bf16_f32 v92, v92, v95
	ds_write_b16 v107, v92 offset:272
	ds_write_b16_d16_hi v107, v92 offset:544
	v_mul_f32_e32 v96, v3, v96
	v_mul_f32_e32 v99, v4, v99
	v_cvt_pk_bf16_f32 v92, v94, v97
	ds_write_b16 v107, v92 offset:816
	ds_write_b16_d16_hi v107, v92 offset:1088
	v_mul_f32_e32 v93, v6, v93
	v_mul_f32_e32 v98, v5, v98
	v_cvt_pk_bf16_f32 v92, v96, v99
	ds_write_b16 v107, v92 offset:1360
	ds_write_b16_d16_hi v107, v92 offset:1632
	v_cvt_pk_bf16_f32 v92, v93, v98
	ds_write_b16 v107, v92
	ds_write_b16_d16_hi v107, v92 offset:1904
	v_lshl_add_u32 v96, v147, 5, s7
	ds_read_b128 v[92:95], v96
	ds_read_b128 v[96:99], v96 offset:16
	s_waitcnt lgkmcnt(1)
	v_add_f32_e32 v92, v92, v93
	v_add_f32_e32 v93, v94, v95
	v_add_f32_e32 v92, v92, v93
	s_waitcnt lgkmcnt(0)
	v_add_f32_e32 v93, v96, v97
	v_add_f32_e32 v92, v92, v93
	v_add_f32_e32 v93, v98, v99
	v_add_f32_e32 v92, v93, v92
	v_fmamk_f32 v92, v92, 0x3b000000, v235
	v_rsq_f32_e32 v92, v92
	s_nop 0
	v_mul_f32_e32 v83, v92, v83
	v_mul_f32_e32 v84, v92, v84
	v_mul_f32_e32 v83, v7, v83
	v_mul_f32_e32 v86, v92, v86
	v_mul_f32_e32 v85, v92, v85
	v_mul_f32_e32 v89, v92, v89
	v_mul_f32_e32 v88, v92, v88
	v_mul_f32_e32 v91, v92, v91
	v_mul_f32_e32 v90, v92, v90
	v_xor_b32_e32 v92, v232, v147
	v_lshlrev_b32_e32 v92, 1, v92
	v_mul_f32_e32 v86, v8, v86
	v_add3_u32 v92, s20, v92, v0
	v_mul_f32_e32 v85, v9, v85
	v_mul_f32_e32 v89, v2, v89
	v_cvt_pk_bf16_f32 v83, v83, v86
	ds_write_b16 v92, v83 offset:272
	ds_write_b16_d16_hi v92, v83 offset:544
	v_mul_f32_e32 v88, v3, v88
	v_mul_f32_e32 v91, v4, v91
	v_cvt_pk_bf16_f32 v83, v85, v89
	ds_write_b16 v92, v83 offset:816
	ds_write_b16_d16_hi v92, v83 offset:1088
	v_mul_f32_e32 v84, v6, v84
	v_mul_f32_e32 v90, v5, v90
	v_cvt_pk_bf16_f32 v83, v88, v91
	ds_write_b16 v92, v83 offset:1360
	ds_write_b16_d16_hi v92, v83 offset:1632
	v_cvt_pk_bf16_f32 v83, v84, v90
	ds_write_b16 v92, v83
	ds_write_b16_d16_hi v92, v83 offset:1904
	v_lshl_add_u32 v83, v146, 5, s7
	ds_read_b128 v[88:91], v83
	ds_read_b128 v[92:95], v83 offset:16
	s_waitcnt lgkmcnt(1)
	v_add_f32_e32 v83, v88, v89
	v_add_f32_e32 v84, v90, v91
	v_add_f32_e32 v83, v83, v84
	s_waitcnt lgkmcnt(0)
	v_add_f32_e32 v84, v92, v93
	v_add_f32_e32 v83, v83, v84
	v_add_f32_e32 v84, v94, v95
	v_add_f32_e32 v83, v84, v83
	v_fmamk_f32 v83, v83, 0x3b000000, v235
	v_rsq_f32_e32 v83, v83
	s_nop 0
	v_mul_f32_e32 v75, v83, v75
	v_mul_f32_e32 v76, v83, v76
	v_mul_f32_e32 v75, v7, v75
	v_mul_f32_e32 v78, v83, v78
	v_mul_f32_e32 v77, v83, v77
	v_mul_f32_e32 v80, v83, v80
	v_mul_f32_e32 v79, v83, v79
	v_mul_f32_e32 v82, v83, v82
	v_mul_f32_e32 v81, v83, v81
	v_xor_b32_e32 v83, v232, v146
	v_lshlrev_b32_e32 v83, 1, v83
	v_mul_f32_e32 v78, v8, v78
	v_add3_u32 v83, s20, v83, v0
	v_mul_f32_e32 v77, v9, v77
	v_mul_f32_e32 v80, v2, v80
	v_cvt_pk_bf16_f32 v75, v75, v78
	ds_write_b16 v83, v75 offset:272
	ds_write_b16_d16_hi v83, v75 offset:544
	v_mul_f32_e32 v79, v3, v79
	v_mul_f32_e32 v82, v4, v82
	v_cvt_pk_bf16_f32 v75, v77, v80
	ds_write_b16 v83, v75 offset:816
	ds_write_b16_d16_hi v83, v75 offset:1088
	v_mul_f32_e32 v76, v6, v76
	v_mul_f32_e32 v81, v5, v81
	v_cvt_pk_bf16_f32 v75, v79, v82
	ds_write_b16 v83, v75 offset:1360
	ds_write_b16_d16_hi v83, v75 offset:1632
	v_cvt_pk_bf16_f32 v75, v76, v81
	ds_write_b16 v83, v75
	ds_write_b16_d16_hi v83, v75 offset:1904
	v_lshl_add_u32 v75, v145, 5, s7
	ds_read_b128 v[76:79], v75
	ds_read_b128 v[80:83], v75 offset:16
	s_waitcnt lgkmcnt(1)
	v_add_f32_e32 v75, v76, v77
	v_add_f32_e32 v76, v78, v79
	v_add_f32_e32 v75, v75, v76
	s_waitcnt lgkmcnt(0)
	v_add_f32_e32 v76, v80, v81
	v_add_f32_e32 v75, v75, v76
	v_add_f32_e32 v76, v82, v83
	v_add_f32_e32 v75, v76, v75
	v_fmamk_f32 v75, v75, 0x3b000000, v235
	v_rsq_f32_e32 v75, v75
	s_nop 0
	v_mul_f32_e32 v67, v75, v67
	v_mul_f32_e32 v68, v75, v68
	v_mul_f32_e32 v67, v7, v67
	v_mul_f32_e32 v70, v75, v70
	v_mul_f32_e32 v69, v75, v69
	v_mul_f32_e32 v72, v75, v72
	v_mul_f32_e32 v71, v75, v71
	v_mul_f32_e32 v74, v75, v74
	v_mul_f32_e32 v73, v75, v73
	v_xor_b32_e32 v75, v232, v145
	v_lshlrev_b32_e32 v75, 1, v75
	v_mul_f32_e32 v70, v8, v70
	v_add3_u32 v75, s20, v75, v0
	v_mul_f32_e32 v69, v9, v69
	v_mul_f32_e32 v72, v2, v72
	v_cvt_pk_bf16_f32 v67, v67, v70
	ds_write_b16 v75, v67 offset:272
	ds_write_b16_d16_hi v75, v67 offset:544
	v_mul_f32_e32 v71, v3, v71
	v_mul_f32_e32 v74, v4, v74
	v_cvt_pk_bf16_f32 v67, v69, v72
	ds_write_b16 v75, v67 offset:816
	ds_write_b16_d16_hi v75, v67 offset:1088
	v_mul_f32_e32 v68, v6, v68
	v_mul_f32_e32 v73, v5, v73
	v_cvt_pk_bf16_f32 v67, v71, v74
	ds_write_b16 v75, v67 offset:1360
	ds_write_b16_d16_hi v75, v67 offset:1632
	v_cvt_pk_bf16_f32 v67, v68, v73
	ds_write_b16 v75, v67
	ds_write_b16_d16_hi v75, v67 offset:1904
	v_lshl_add_u32 v67, v143, 5, s7
	ds_read_b128 v[68:71], v67
	ds_read_b128 v[72:75], v67 offset:16
	s_waitcnt lgkmcnt(1)
	v_add_f32_e32 v67, v68, v69
	v_add_f32_e32 v68, v70, v71
	v_add_f32_e32 v67, v67, v68
	s_waitcnt lgkmcnt(0)
	v_add_f32_e32 v68, v72, v73
	v_add_f32_e32 v67, v67, v68
	v_add_f32_e32 v68, v74, v75
	v_add_f32_e32 v67, v68, v67
	v_fmamk_f32 v67, v67, 0x3b000000, v235
	v_rsq_f32_e32 v67, v67
	s_nop 0
	v_mul_f32_e32 v59, v67, v59
	v_mul_f32_e32 v60, v67, v60
	v_mul_f32_e32 v59, v7, v59
	v_mul_f32_e32 v62, v67, v62
	v_mul_f32_e32 v61, v67, v61
	v_mul_f32_e32 v64, v67, v64
	v_mul_f32_e32 v63, v67, v63
	v_mul_f32_e32 v66, v67, v66
	v_mul_f32_e32 v65, v67, v65
	v_xor_b32_e32 v67, v232, v143
	v_lshlrev_b32_e32 v67, 1, v67
	v_mul_f32_e32 v62, v8, v62
	v_add3_u32 v67, s20, v67, v0
	v_mul_f32_e32 v61, v9, v61
	v_mul_f32_e32 v64, v2, v64
	v_cvt_pk_bf16_f32 v59, v59, v62
	ds_write_b16 v67, v59 offset:272
	ds_write_b16_d16_hi v67, v59 offset:544
	v_mul_f32_e32 v63, v3, v63
	v_mul_f32_e32 v66, v4, v66
	v_cvt_pk_bf16_f32 v59, v61, v64
	ds_write_b16 v67, v59 offset:816
	ds_write_b16_d16_hi v67, v59 offset:1088
	v_mul_f32_e32 v60, v6, v60
	v_mul_f32_e32 v65, v5, v65
	v_cvt_pk_bf16_f32 v59, v63, v66
	ds_write_b16 v67, v59 offset:1360
	ds_write_b16_d16_hi v67, v59 offset:1632
	v_cvt_pk_bf16_f32 v59, v60, v65
	ds_write_b16 v67, v59
	ds_write_b16_d16_hi v67, v59 offset:1904
	v_lshl_add_u32 v59, v134, 5, s7
	ds_read_b128 v[60:63], v59
	ds_read_b128 v[64:67], v59 offset:16
	s_waitcnt lgkmcnt(1)
	v_add_f32_e32 v59, v60, v61
	v_add_f32_e32 v60, v62, v63
	v_add_f32_e32 v59, v59, v60
	s_waitcnt lgkmcnt(0)
	v_add_f32_e32 v60, v64, v65
	v_add_f32_e32 v59, v59, v60
	v_add_f32_e32 v60, v66, v67
	v_add_f32_e32 v59, v60, v59
	v_fmamk_f32 v59, v59, 0x3b000000, v235
	v_rsq_f32_e32 v59, v59
	s_nop 0
	v_mul_f32_e32 v51, v59, v51
	v_mul_f32_e32 v52, v59, v52
	v_mul_f32_e32 v51, v7, v51
	v_mul_f32_e32 v54, v59, v54
	v_mul_f32_e32 v53, v59, v53
	v_mul_f32_e32 v56, v59, v56
	v_mul_f32_e32 v55, v59, v55
	v_mul_f32_e32 v58, v59, v58
	v_mul_f32_e32 v57, v59, v57
	v_xor_b32_e32 v59, v232, v134
	v_lshlrev_b32_e32 v59, 1, v59
	v_mul_f32_e32 v54, v8, v54
	v_add3_u32 v59, s20, v59, v0
	v_mul_f32_e32 v53, v9, v53
	v_mul_f32_e32 v56, v2, v56
	v_cvt_pk_bf16_f32 v51, v51, v54
	ds_write_b16 v59, v51 offset:272
	ds_write_b16_d16_hi v59, v51 offset:544
	v_mul_f32_e32 v55, v3, v55
	v_mul_f32_e32 v58, v4, v58
	v_cvt_pk_bf16_f32 v51, v53, v56
	ds_write_b16 v59, v51 offset:816
	ds_write_b16_d16_hi v59, v51 offset:1088
	v_mul_f32_e32 v52, v6, v52
	v_mul_f32_e32 v57, v5, v57
	v_cvt_pk_bf16_f32 v51, v55, v58
	ds_write_b16 v59, v51 offset:1360
	ds_write_b16_d16_hi v59, v51 offset:1632
	v_cvt_pk_bf16_f32 v51, v52, v57
	ds_write_b16 v59, v51
	ds_write_b16_d16_hi v59, v51 offset:1904
	v_lshl_add_u32 v51, v133, 5, s7
	ds_read_b128 v[52:55], v51
	ds_read_b128 v[56:59], v51 offset:16
	s_waitcnt lgkmcnt(1)
	v_add_f32_e32 v51, v52, v53
	v_add_f32_e32 v52, v54, v55
	v_add_f32_e32 v51, v51, v52
	s_waitcnt lgkmcnt(0)
	v_add_f32_e32 v52, v56, v57
	v_add_f32_e32 v51, v51, v52
	v_add_f32_e32 v52, v58, v59
	v_add_f32_e32 v51, v52, v51
	v_fmamk_f32 v51, v51, 0x3b000000, v235
	v_rsq_f32_e32 v51, v51
	s_nop 0
	v_mul_f32_e32 v42, v51, v42
	v_mul_f32_e32 v43, v51, v43
	v_mul_f32_e32 v42, v7, v42
	v_mul_f32_e32 v45, v51, v45
	v_mul_f32_e32 v44, v51, v44
	v_mul_f32_e32 v47, v51, v47
	v_mul_f32_e32 v46, v51, v46
	v_mul_f32_e32 v50, v51, v50
	v_mul_f32_e32 v48, v51, v48
	v_xor_b32_e32 v51, v232, v133
	v_lshlrev_b32_e32 v51, 1, v51
	v_mul_f32_e32 v45, v8, v45
	v_add3_u32 v51, s20, v51, v0
	v_mul_f32_e32 v44, v9, v44
	v_mul_f32_e32 v47, v2, v47
	v_cvt_pk_bf16_f32 v42, v42, v45
	ds_write_b16 v51, v42 offset:272
	ds_write_b16_d16_hi v51, v42 offset:544
	v_mul_f32_e32 v46, v3, v46
	v_mul_f32_e32 v50, v4, v50
	v_cvt_pk_bf16_f32 v42, v44, v47
	ds_write_b16 v51, v42 offset:816
	ds_write_b16_d16_hi v51, v42 offset:1088
	v_mul_f32_e32 v43, v6, v43
	v_mul_f32_e32 v48, v5, v48
	v_cvt_pk_bf16_f32 v42, v46, v50
	ds_write_b16 v51, v42 offset:1360
	ds_write_b16_d16_hi v51, v42 offset:1632
	v_cvt_pk_bf16_f32 v42, v43, v48
	ds_write_b16 v51, v42
	ds_write_b16_d16_hi v51, v42 offset:1904
	v_lshl_add_u32 v46, v132, 5, s7
	ds_read_b128 v[42:45], v46
	ds_read_b128 v[50:53], v46 offset:16
	s_waitcnt lgkmcnt(1)
	v_add_f32_e32 v42, v42, v43
	v_add_f32_e32 v43, v44, v45
	v_add_f32_e32 v42, v42, v43
	s_waitcnt lgkmcnt(0)
	v_add_f32_e32 v43, v50, v51
	v_add_f32_e32 v42, v42, v43
	v_add_f32_e32 v43, v52, v53
	v_add_f32_e32 v42, v43, v42
	v_fmamk_f32 v42, v42, 0x3b000000, v235
	v_rsq_f32_e32 v42, v42
	s_nop 0
	v_mul_f32_e32 v34, v42, v34
	v_mul_f32_e32 v35, v42, v35
	v_mul_f32_e32 v34, v7, v34
	v_mul_f32_e32 v37, v42, v37
	v_mul_f32_e32 v36, v42, v36
	v_mul_f32_e32 v39, v42, v39
	v_mul_f32_e32 v38, v42, v38
	v_mul_f32_e32 v41, v42, v41
	v_mul_f32_e32 v40, v42, v40
	v_xor_b32_e32 v42, v232, v132
	v_lshlrev_b32_e32 v42, 1, v42
	v_mul_f32_e32 v37, v8, v37
	v_add3_u32 v42, s20, v42, v0
	v_mul_f32_e32 v36, v9, v36
	v_mul_f32_e32 v39, v2, v39
	v_cvt_pk_bf16_f32 v34, v34, v37
	ds_write_b16 v42, v34 offset:272
	ds_write_b16_d16_hi v42, v34 offset:544
	v_mul_f32_e32 v38, v3, v38
	v_mul_f32_e32 v41, v4, v41
	v_cvt_pk_bf16_f32 v34, v36, v39
	ds_write_b16 v42, v34 offset:816
	ds_write_b16_d16_hi v42, v34 offset:1088
	v_mul_f32_e32 v35, v6, v35
	v_mul_f32_e32 v40, v5, v40
	v_cvt_pk_bf16_f32 v34, v38, v41
	ds_write_b16 v42, v34 offset:1360
	ds_write_b16_d16_hi v42, v34 offset:1632
	v_cvt_pk_bf16_f32 v34, v35, v40
	ds_write_b16 v42, v34
	ds_write_b16_d16_hi v42, v34 offset:1904
	v_lshl_add_u32 v38, v128, 5, s7
	ds_read_b128 v[34:37], v38
	ds_read_b128 v[38:41], v38 offset:16
	s_waitcnt lgkmcnt(1)
	v_add_f32_e32 v34, v34, v35
	v_add_f32_e32 v35, v36, v37
	v_add_f32_e32 v34, v34, v35
	s_waitcnt lgkmcnt(0)
	v_add_f32_e32 v35, v38, v39
	v_add_f32_e32 v34, v34, v35
	v_add_f32_e32 v35, v40, v41
	v_add_f32_e32 v34, v35, v34
	v_fmamk_f32 v34, v34, 0x3b000000, v235
	v_rsq_f32_e32 v34, v34
	s_nop 0
	v_mul_f32_e32 v26, v34, v26
	v_mul_f32_e32 v27, v34, v27
	v_mul_f32_e32 v26, v7, v26
	v_mul_f32_e32 v29, v34, v29
	v_mul_f32_e32 v28, v34, v28
	v_mul_f32_e32 v31, v34, v31
	v_mul_f32_e32 v30, v34, v30
	v_mul_f32_e32 v33, v34, v33
	v_mul_f32_e32 v32, v34, v32
	v_xor_b32_e32 v34, v232, v128
	v_lshlrev_b32_e32 v34, 1, v34
	v_mul_f32_e32 v29, v8, v29
	v_add3_u32 v34, s20, v34, v0
	v_mul_f32_e32 v28, v9, v28
	v_mul_f32_e32 v31, v2, v31
	v_cvt_pk_bf16_f32 v26, v26, v29
	ds_write_b16 v34, v26 offset:272
	ds_write_b16_d16_hi v34, v26 offset:544
	v_mul_f32_e32 v30, v3, v30
	v_mul_f32_e32 v33, v4, v33
	v_cvt_pk_bf16_f32 v26, v28, v31
	ds_write_b16 v34, v26 offset:816
	ds_write_b16_d16_hi v34, v26 offset:1088
	v_mul_f32_e32 v27, v6, v27
	v_mul_f32_e32 v32, v5, v32
	v_cvt_pk_bf16_f32 v26, v30, v33
	ds_write_b16 v34, v26 offset:1360
	ds_write_b16_d16_hi v34, v26 offset:1632
	v_cvt_pk_bf16_f32 v26, v27, v32
	ds_write_b16 v34, v26
	ds_write_b16_d16_hi v34, v26 offset:1904
	v_lshl_add_u32 v30, v87, 5, s7
	ds_read_b128 v[26:29], v30
	ds_read_b128 v[30:33], v30 offset:16
	s_waitcnt lgkmcnt(1)
	v_add_f32_e32 v26, v26, v27
	v_add_f32_e32 v27, v28, v29
	v_add_f32_e32 v26, v26, v27
	s_waitcnt lgkmcnt(0)
	v_add_f32_e32 v27, v30, v31
	v_add_f32_e32 v26, v26, v27
	v_add_f32_e32 v27, v32, v33
	v_add_f32_e32 v26, v27, v26
	v_fmamk_f32 v26, v26, 0x3b000000, v235
	v_rsq_f32_e32 v26, v26
	s_nop 0
	v_mul_f32_e32 v18, v26, v18
	v_mul_f32_e32 v19, v26, v19
	v_mul_f32_e32 v18, v7, v18
	v_mul_f32_e32 v21, v26, v21
	v_mul_f32_e32 v20, v26, v20
	v_mul_f32_e32 v23, v26, v23
	v_mul_f32_e32 v22, v26, v22
	v_mul_f32_e32 v25, v26, v25
	v_mul_f32_e32 v24, v26, v24
	v_xor_b32_e32 v26, v232, v87
	v_lshlrev_b32_e32 v26, 1, v26
	v_mul_f32_e32 v21, v8, v21
	v_add3_u32 v26, s20, v26, v0
	v_mul_f32_e32 v20, v9, v20
	v_mul_f32_e32 v23, v2, v23
	v_cvt_pk_bf16_f32 v18, v18, v21
	ds_write_b16 v26, v18 offset:272
	ds_write_b16_d16_hi v26, v18 offset:544
	v_mul_f32_e32 v22, v3, v22
	v_mul_f32_e32 v25, v4, v25
	v_cvt_pk_bf16_f32 v18, v20, v23
	ds_write_b16 v26, v18 offset:816
	ds_write_b16_d16_hi v26, v18 offset:1088
	v_mul_f32_e32 v19, v6, v19
	v_mul_f32_e32 v24, v5, v24
	v_cvt_pk_bf16_f32 v18, v22, v25
	ds_write_b16 v26, v18 offset:1360
	ds_write_b16_d16_hi v26, v18 offset:1632
	v_cvt_pk_bf16_f32 v18, v19, v24
	ds_write_b16 v26, v18
	ds_write_b16_d16_hi v26, v18 offset:1904
	v_lshl_add_u32 v22, v49, 5, s7
	ds_read_b128 v[18:21], v22
	ds_read_b128 v[22:25], v22 offset:16
	s_waitcnt lgkmcnt(1)
	v_add_f32_e32 v18, v18, v19
	v_add_f32_e32 v19, v20, v21
	v_add_f32_e32 v18, v18, v19
	s_waitcnt lgkmcnt(0)
	v_add_f32_e32 v19, v22, v23
	v_add_f32_e32 v18, v18, v19
	v_add_f32_e32 v19, v24, v25
	v_add_f32_e32 v18, v19, v18
	v_fmamk_f32 v18, v18, 0x3b000000, v235
	v_rsq_f32_e32 v18, v18
	s_nop 0
	v_mul_f32_e32 v10, v18, v10
	v_mul_f32_e32 v7, v7, v10
	v_mul_f32_e32 v10, v18, v13
	v_mul_f32_e32 v8, v8, v10
	v_mul_f32_e32 v10, v18, v12
	v_mul_f32_e32 v9, v9, v10
	v_mul_f32_e32 v10, v18, v15
	v_mul_f32_e32 v2, v2, v10
	v_mul_f32_e32 v10, v18, v14
	v_mul_f32_e32 v3, v3, v10
	v_mul_f32_e32 v10, v18, v17
	v_mul_f32_e32 v11, v18, v11
	v_mul_f32_e32 v4, v4, v10
	v_mul_f32_e32 v10, v18, v16
	v_mul_f32_e32 v6, v6, v11
	v_mul_f32_e32 v5, v5, v10
	v_xor_b32_e32 v10, v232, v49
	v_lshlrev_b32_e32 v10, 1, v10
	v_add3_u32 v0, s20, v10, v0
	v_cvt_pk_bf16_f32 v2, v6, v2
	ds_write_b16 v0, v2
	ds_write_b16_d16_hi v0, v2 offset:1088
	v_cvt_pk_bf16_f32 v2, v7, v3
	ds_write_b16 v0, v2 offset:272
	ds_write_b16_d16_hi v0, v2 offset:1360
	v_cvt_pk_bf16_f32 v2, v8, v4
	ds_write_b16 v0, v2 offset:544
	ds_write_b16_d16_hi v0, v2 offset:1632
	v_cvt_pk_bf16_f32 v2, v9, v5
	ds_write_b16 v0, v2 offset:816
	ds_write_b16_d16_hi v0, v2 offset:1904
	v_lshlrev_b32_e32 v0, 4, v106
	v_lshlrev_b32_e32 v4, 2, v106
	v_lshl_add_u64 v[2:3], s[4:5], 0, v[0:1]
	v_lshl_or_b32 v54, s12, 7, v4
	v_lshlrev_b32_e32 v4, 8, v105
	v_mov_b32_e32 v5, v1
	v_lshl_add_u64 v[82:83], v[2:3], 0, v[4:5]
	s_mov_b64 s[4:5], 0x1620000
	v_lshl_add_u64 v[6:7], v[82:83], 0, s[4:5]
	s_mov_b32 s4, 0x1620000
	v_add_co_u32_e32 v2, vcc, s4, v82
	s_waitcnt lgkmcnt(0)
	s_nop 0
	v_addc_co_u32_e32 v3, vcc, 0, v83, vcc
	s_barrier
	global_load_dwordx4 v[2:5], v[2:3], off
	s_nop 0
	global_load_dwordx4 v[50:53], v[6:7], off offset:32
	v_mul_u32_u24_e32 v8, 0x110, v105
	v_and_b32_e32 v42, 16, v105
	v_xor_b32_e32 v0, v42, v0
	v_add3_u32 v0, s20, v8, v0
	ds_read_b128 v[42:45], v0 offset:8736
	ds_read_b128 v[46:49], v0
	ds_read_b128 v[38:41], v0 offset:32
	s_waitcnt vmcnt(1) lgkmcnt(1)
	v_mfma_f32_32x32x16_bf16 v[18:33], v[2:5], v[46:49], 0
	ds_read_b128 v[34:37], v0 offset:8704
	v_ashrrev_i32_e32 v55, 31, v54
	v_lshl_add_u64 v[98:99], v[54:55], 2, s[16:17]
	s_mov_b32 s4, 0x1622000
	v_mfma_f32_32x32x16_bf16 v[2:17], v[2:5], v[42:45], 0
	s_waitcnt vmcnt(0) lgkmcnt(1)
	v_mfma_f32_32x32x16_bf16 v[18:33], v[50:53], v[38:41], v[18:33]
	s_waitcnt lgkmcnt(0)
	v_mfma_f32_32x32x16_bf16 v[2:17], v[50:53], v[34:37], v[2:17]
	global_load_dwordx4 v[50:53], v[98:99], off
	global_load_dwordx4 v[54:57], v[98:99], off offset:32
	global_load_dwordx4 v[58:61], v[98:99], off offset:64
	global_load_dwordx4 v[62:65], v[98:99], off offset:96
	s_nop 5
	v_mov_b32_e32 v66, v18
	s_nop 0
	v_mov_b32_e32 v67, v2
	v_mov_b32_e32 v2, v19
	s_waitcnt vmcnt(3)
	v_pk_add_f32 v[2:3], v[2:3], v[50:51] op_sel:[0,1]
	s_nop 0
	v_cvt_pk_bf16_f32 v108, v2, v3
	v_mov_b32_e32 v2, v20
	v_mov_b32_e32 v3, v4
	v_pk_add_f32 v[2:3], v[2:3], v[52:53] op_sel_hi:[1,0]
	v_mov_b32_e32 v4, v21
	v_cvt_pk_bf16_f32 v109, v2, v3
	v_mov_b32_e32 v2, v53
	v_pk_add_f32 v[2:3], v[4:5], v[2:3] op_sel_hi:[1,0]
	v_pk_add_f32 v[66:67], v[66:67], v[50:51] op_sel_hi:[1,0]
	v_cvt_pk_bf16_f32 v110, v2, v3
	v_mov_b32_e32 v2, v22
	v_mov_b32_e32 v3, v6
	s_waitcnt vmcnt(2)
	v_pk_add_f32 v[2:3], v[2:3], v[54:55] op_sel_hi:[1,0]
	v_mov_b32_e32 v6, v23
	v_cvt_pk_bf16_f32 v111, v2, v3
	v_pk_add_f32 v[2:3], v[6:7], v[54:55] op_sel:[0,1]
	v_add_co_u32_e32 v6, vcc, s4, v82
	v_cvt_pk_bf16_f32 v112, v2, v3
	v_mov_b32_e32 v2, v24
	v_mov_b32_e32 v3, v8
	v_pk_add_f32 v[2:3], v[2:3], v[56:57] op_sel_hi:[1,0]
	v_mov_b32_e32 v8, v25
	v_cvt_pk_bf16_f32 v113, v2, v3
	v_mov_b32_e32 v2, v57
	v_pk_add_f32 v[2:3], v[8:9], v[2:3] op_sel_hi:[1,0]
	v_addc_co_u32_e32 v7, vcc, 0, v83, vcc
	v_cvt_pk_bf16_f32 v114, v2, v3
	v_mov_b32_e32 v2, v26
	v_mov_b32_e32 v3, v10
	s_waitcnt vmcnt(1)
	v_pk_add_f32 v[2:3], v[2:3], v[58:59] op_sel_hi:[1,0]
	v_mov_b32_e32 v10, v27
	v_cvt_pk_bf16_f32 v115, v2, v3
	v_pk_add_f32 v[2:3], v[10:11], v[58:59] op_sel:[0,1]
	v_cvt_pk_bf16_f32 v107, v66, v67
	v_cvt_pk_bf16_f32 v116, v2, v3
	v_mov_b32_e32 v2, v28
	v_mov_b32_e32 v3, v12
	v_pk_add_f32 v[2:3], v[2:3], v[60:61] op_sel_hi:[1,0]
	v_mov_b32_e32 v12, v29
	v_cvt_pk_bf16_f32 v117, v2, v3
	v_mov_b32_e32 v2, v61
	v_pk_add_f32 v[2:3], v[12:13], v[2:3] op_sel_hi:[1,0]
	s_mov_b32 s4, 0x1624000
	v_cvt_pk_bf16_f32 v118, v2, v3
	v_mov_b32_e32 v2, v30
	v_mov_b32_e32 v3, v14
	s_waitcnt vmcnt(0)
	v_pk_add_f32 v[2:3], v[2:3], v[62:63] op_sel_hi:[1,0]
	v_mov_b32_e32 v14, v31
	v_cvt_pk_bf16_f32 v119, v2, v3
	v_pk_add_f32 v[2:3], v[14:15], v[62:63] op_sel:[0,1]
	s_nop 0
	v_cvt_pk_bf16_f32 v120, v2, v3
	v_mov_b32_e32 v2, v32
	v_mov_b32_e32 v3, v16
	v_pk_add_f32 v[2:3], v[2:3], v[64:65] op_sel_hi:[1,0]
	v_mov_b32_e32 v16, v33
	v_cvt_pk_bf16_f32 v121, v2, v3
	v_mov_b32_e32 v2, v65
	v_pk_add_f32 v[2:3], v[16:17], v[2:3] op_sel_hi:[1,0]
	s_nop 0
	v_cvt_pk_bf16_f32 v122, v2, v3
	global_load_dwordx4 v[2:5], v[6:7], off
	global_load_dwordx4 v[50:53], v[6:7], off offset:32
	global_load_dwordx4 v[54:57], v[6:7], off offset:64
	global_load_dwordx4 v[66:69], v[6:7], off offset:96
	s_waitcnt vmcnt(3)
	v_mfma_f32_32x32x16_bf16 v[18:33], v[2:5], v[46:49], 0
	ds_read_b128 v[62:65], v0 offset:64
	ds_read_b128 v[58:61], v0 offset:8800
	v_mfma_f32_32x32x16_bf16 v[2:17], v[2:5], v[42:45], 0
	s_waitcnt vmcnt(2)
	v_mfma_f32_32x32x16_bf16 v[18:33], v[50:53], v[38:41], v[18:33]
	v_mfma_f32_32x32x16_bf16 v[2:17], v[50:53], v[34:37], v[2:17]
	s_waitcnt vmcnt(1) lgkmcnt(1)
	v_mfma_f32_32x32x16_bf16 v[18:33], v[54:57], v[62:65], v[18:33]
	s_waitcnt lgkmcnt(0)
	v_mfma_f32_32x32x16_bf16 v[2:17], v[54:57], v[58:61], v[2:17]
	ds_read_b128 v[50:53], v0 offset:96
	ds_read_b128 v[54:57], v0 offset:8768
	s_waitcnt vmcnt(0) lgkmcnt(1)
	v_mfma_f32_32x32x16_bf16 v[18:33], v[66:69], v[50:53], v[18:33]
	s_waitcnt lgkmcnt(0)
	v_mfma_f32_32x32x16_bf16 v[2:17], v[66:69], v[54:57], v[2:17]
	global_load_dwordx4 v[66:69], v[98:99], off offset:128
	global_load_dwordx4 v[70:73], v[98:99], off offset:160
	global_load_dwordx4 v[74:77], v[98:99], off offset:192
	global_load_dwordx4 v[78:81], v[98:99], off offset:224
	s_nop 5
	v_mov_b32_e32 v84, v18
	s_nop 0
	v_mov_b32_e32 v85, v2
	v_mov_b32_e32 v2, v19
	s_waitcnt vmcnt(3)
	v_pk_add_f32 v[2:3], v[2:3], v[66:67] op_sel:[0,1]
	s_nop 0
	v_cvt_pk_bf16_f32 v124, v2, v3
	v_mov_b32_e32 v2, v20
	v_mov_b32_e32 v3, v4
	v_pk_add_f32 v[2:3], v[2:3], v[68:69] op_sel_hi:[1,0]
	v_mov_b32_e32 v4, v21
	v_cvt_pk_bf16_f32 v125, v2, v3
	v_mov_b32_e32 v2, v69
	v_pk_add_f32 v[2:3], v[4:5], v[2:3] op_sel_hi:[1,0]
	v_pk_add_f32 v[84:85], v[84:85], v[66:67] op_sel_hi:[1,0]
	v_cvt_pk_bf16_f32 v126, v2, v3
	v_mov_b32_e32 v2, v22
	v_mov_b32_e32 v3, v6
	s_waitcnt vmcnt(2)
	v_pk_add_f32 v[2:3], v[2:3], v[70:71] op_sel_hi:[1,0]
	v_mov_b32_e32 v6, v23
	v_cvt_pk_bf16_f32 v127, v2, v3
	v_pk_add_f32 v[2:3], v[6:7], v[70:71] op_sel:[0,1]
	v_cvt_pk_bf16_f32 v123, v84, v85
	v_cvt_pk_bf16_f32 v128, v2, v3
	v_mov_b32_e32 v2, v24
	v_mov_b32_e32 v3, v8
	v_pk_add_f32 v[2:3], v[2:3], v[72:73] op_sel_hi:[1,0]
	v_mov_b32_e32 v8, v25
	v_cvt_pk_bf16_f32 v129, v2, v3
	v_mov_b32_e32 v2, v73
	v_pk_add_f32 v[2:3], v[8:9], v[2:3] op_sel_hi:[1,0]
	s_nop 0
	v_cvt_pk_bf16_f32 v130, v2, v3
	v_mov_b32_e32 v2, v26
	v_mov_b32_e32 v3, v10
	s_waitcnt vmcnt(1)
	v_pk_add_f32 v[2:3], v[2:3], v[74:75] op_sel_hi:[1,0]
	v_mov_b32_e32 v10, v27
	v_cvt_pk_bf16_f32 v131, v2, v3
	v_pk_add_f32 v[2:3], v[10:11], v[74:75] op_sel:[0,1]
	s_nop 0
	v_cvt_pk_bf16_f32 v132, v2, v3
	v_mov_b32_e32 v2, v28
	v_mov_b32_e32 v3, v12
	v_pk_add_f32 v[2:3], v[2:3], v[76:77] op_sel_hi:[1,0]
	v_mov_b32_e32 v12, v29
	v_cvt_pk_bf16_f32 v133, v2, v3
	v_mov_b32_e32 v2, v77
	v_pk_add_f32 v[2:3], v[12:13], v[2:3] op_sel_hi:[1,0]
	s_nop 0
	v_cvt_pk_bf16_f32 v134, v2, v3
	v_mov_b32_e32 v2, v30
	v_mov_b32_e32 v3, v14
	s_waitcnt vmcnt(0)
	v_pk_add_f32 v[2:3], v[2:3], v[78:79] op_sel_hi:[1,0]
	v_mov_b32_e32 v14, v31
	v_cvt_pk_bf16_f32 v135, v2, v3
	v_pk_add_f32 v[2:3], v[14:15], v[78:79] op_sel:[0,1]
	s_nop 0
	v_cvt_pk_bf16_f32 v136, v2, v3
	v_mov_b32_e32 v2, v32
	v_mov_b32_e32 v3, v16
	v_pk_add_f32 v[2:3], v[2:3], v[80:81] op_sel_hi:[1,0]
	v_mov_b32_e32 v16, v33
	v_cvt_pk_bf16_f32 v137, v2, v3
	v_mov_b32_e32 v2, v81
	v_pk_add_f32 v[2:3], v[16:17], v[2:3] op_sel_hi:[1,0]
	s_nop 0
	v_cvt_pk_bf16_f32 v138, v2, v3
	v_add_co_u32_e32 v2, vcc, s4, v82
	s_mov_b32 s4, 0x1626000
	s_nop 0
	v_addc_co_u32_e32 v3, vcc, 0, v83, vcc
	global_load_dwordx4 v[18:21], v[2:3], off
	global_load_dwordx4 v[66:69], v[2:3], off offset:32
	global_load_dwordx4 v[70:73], v[2:3], off offset:64
	global_load_dwordx4 v[74:77], v[2:3], off offset:96
	global_load_dwordx4 v[78:81], v[2:3], off offset:128
	global_load_dwordx4 v[84:87], v[2:3], off offset:160
	s_waitcnt vmcnt(5)
	v_mfma_f32_32x32x16_bf16 v[2:17], v[18:21], v[46:49], 0
	v_mfma_f32_32x32x16_bf16 v[18:33], v[18:21], v[42:45], 0
	s_waitcnt vmcnt(4)
	v_mfma_f32_32x32x16_bf16 v[2:17], v[66:69], v[38:41], v[2:17]
	v_mfma_f32_32x32x16_bf16 v[18:33], v[66:69], v[34:37], v[18:33]
	s_waitcnt vmcnt(3)
	v_mfma_f32_32x32x16_bf16 v[2:17], v[70:73], v[62:65], v[2:17]
	v_mfma_f32_32x32x16_bf16 v[18:33], v[70:73], v[58:61], v[18:33]
	ds_read_b128 v[66:69], v0 offset:128
	ds_read_b128 v[70:73], v0 offset:8864
	s_waitcnt vmcnt(2)
	v_mfma_f32_32x32x16_bf16 v[2:17], v[74:77], v[50:53], v[2:17]
	v_mfma_f32_32x32x16_bf16 v[18:33], v[74:77], v[54:57], v[18:33]
	s_waitcnt vmcnt(1) lgkmcnt(1)
	v_mfma_f32_32x32x16_bf16 v[2:17], v[78:81], v[66:69], v[2:17]
	s_waitcnt lgkmcnt(0)
	v_mfma_f32_32x32x16_bf16 v[18:33], v[78:81], v[70:73], v[18:33]
	ds_read_b128 v[74:77], v0 offset:160
	ds_read_b128 v[78:81], v0 offset:8832
	s_waitcnt vmcnt(0) lgkmcnt(1)
	v_mfma_f32_32x32x16_bf16 v[2:17], v[84:87], v[74:77], v[2:17]
	s_waitcnt lgkmcnt(0)
	v_mfma_f32_32x32x16_bf16 v[18:33], v[84:87], v[78:81], v[18:33]
	global_load_dwordx4 v[84:87], v[98:99], off offset:256
	global_load_dwordx4 v[88:91], v[98:99], off offset:288
	global_load_dwordx4 v[92:95], v[98:99], off offset:320
	global_load_dwordx4 v[156:159], v[98:99], off offset:352
	s_nop 5
	v_mov_b32_e32 v96, v2
	s_nop 0
	v_mov_b32_e32 v97, v18
	v_mov_b32_e32 v18, v3
	s_waitcnt vmcnt(3)
	v_pk_add_f32 v[2:3], v[18:19], v[84:85] op_sel:[0,1]
	s_nop 0
	v_cvt_pk_bf16_f32 v150, v2, v3
	v_mov_b32_e32 v2, v4
	v_mov_b32_e32 v3, v20
	v_pk_add_f32 v[2:3], v[2:3], v[86:87] op_sel_hi:[1,0]
	v_mov_b32_e32 v20, v5
	v_cvt_pk_bf16_f32 v151, v2, v3
	v_mov_b32_e32 v2, v87
	v_pk_add_f32 v[2:3], v[20:21], v[2:3] op_sel_hi:[1,0]
	v_pk_add_f32 v[96:97], v[96:97], v[84:85] op_sel_hi:[1,0]
	v_cvt_pk_bf16_f32 v152, v2, v3
	v_mov_b32_e32 v2, v6
	v_mov_b32_e32 v3, v22
	s_waitcnt vmcnt(2)
	v_pk_add_f32 v[2:3], v[2:3], v[88:89] op_sel_hi:[1,0]
	v_mov_b32_e32 v22, v7
	v_cvt_pk_bf16_f32 v153, v2, v3
	v_pk_add_f32 v[2:3], v[22:23], v[88:89] op_sel:[0,1]
	v_cvt_pk_bf16_f32 v154, v96, v97
	v_cvt_pk_bf16_f32 v146, v2, v3
	v_mov_b32_e32 v2, v8
	v_mov_b32_e32 v3, v24
	v_pk_add_f32 v[2:3], v[2:3], v[90:91] op_sel_hi:[1,0]
	v_mov_b32_e32 v24, v9
	v_cvt_pk_bf16_f32 v147, v2, v3
	v_mov_b32_e32 v2, v91
	v_pk_add_f32 v[2:3], v[24:25], v[2:3] op_sel_hi:[1,0]
	s_nop 0
	v_cvt_pk_bf16_f32 v148, v2, v3
	v_mov_b32_e32 v2, v10
	v_mov_b32_e32 v3, v26
	s_waitcnt vmcnt(1)
	v_pk_add_f32 v[2:3], v[2:3], v[92:93] op_sel_hi:[1,0]
	v_mov_b32_e32 v26, v11
	v_cvt_pk_bf16_f32 v149, v2, v3
	v_pk_add_f32 v[2:3], v[26:27], v[92:93] op_sel:[0,1]
	s_nop 0
	v_cvt_pk_bf16_f32 v142, v2, v3
	v_mov_b32_e32 v2, v12
	v_mov_b32_e32 v3, v28
	v_pk_add_f32 v[2:3], v[2:3], v[94:95] op_sel_hi:[1,0]
	v_mov_b32_e32 v28, v13
	v_cvt_pk_bf16_f32 v143, v2, v3
	v_mov_b32_e32 v2, v95
	v_pk_add_f32 v[2:3], v[28:29], v[2:3] op_sel_hi:[1,0]
	s_nop 0
	v_cvt_pk_bf16_f32 v144, v2, v3
	v_mov_b32_e32 v2, v14
	v_mov_b32_e32 v3, v30
	s_waitcnt vmcnt(0)
	v_pk_add_f32 v[2:3], v[2:3], v[156:157] op_sel_hi:[1,0]
	v_mov_b32_e32 v30, v15
	v_cvt_pk_bf16_f32 v145, v2, v3
	v_pk_add_f32 v[2:3], v[30:31], v[156:157] op_sel:[0,1]
	s_nop 0
	v_cvt_pk_bf16_f32 v139, v2, v3
	v_mov_b32_e32 v2, v16
	v_mov_b32_e32 v3, v32
	v_pk_add_f32 v[2:3], v[2:3], v[158:159] op_sel_hi:[1,0]
	v_mov_b32_e32 v32, v17
	v_cvt_pk_bf16_f32 v140, v2, v3
	v_mov_b32_e32 v2, v159
	v_pk_add_f32 v[2:3], v[32:33], v[2:3] op_sel_hi:[1,0]
	s_nop 0
	v_cvt_pk_bf16_f32 v141, v2, v3
	v_add_co_u32_e32 v2, vcc, s4, v82
	s_ashr_i32 s4, s23, 31
	s_nop 0
	v_addc_co_u32_e32 v3, vcc, 0, v83, vcc
	global_load_dwordx4 v[18:21], v[2:3], off
	global_load_dwordx4 v[82:85], v[2:3], off offset:32
	global_load_dwordx4 v[86:89], v[2:3], off offset:64
	global_load_dwordx4 v[90:93], v[2:3], off offset:96
	global_load_dwordx4 v[94:97], v[2:3], off offset:128
	global_load_dwordx4 v[156:159], v[2:3], off offset:160
	global_load_dwordx4 v[160:163], v[2:3], off offset:192
	global_load_dwordx4 v[164:167], v[2:3], off offset:224
	s_waitcnt vmcnt(7)
	v_mfma_f32_32x32x16_bf16 v[2:17], v[18:21], v[46:49], 0
	s_add_u32 s20, s8, s23
	s_addc_u32 s21, s9, s4
	s_add_u32 s16, s20, 0xffffff88
	s_addc_u32 s17, s21, -1
	s_lshl_b64 s[4:5], s[16:17], 11
	v_mfma_f32_32x32x16_bf16 v[18:33], v[18:21], v[42:45], 0
	s_waitcnt vmcnt(6)
	v_mfma_f32_32x32x16_bf16 v[2:17], v[82:85], v[38:41], v[2:17]
	v_mfma_f32_32x32x16_bf16 v[18:33], v[82:85], v[34:37], v[18:33]
	ds_read_b128 v[34:37], v0 offset:192
	ds_read_b128 v[38:41], v0 offset:8928
	v_or_b32_e32 v82, s6, v105
	v_lshlrev_b32_e32 v82, 1, v82
	v_mul_u32_u24_e32 v83, 0x1040, v106
	v_add3_u32 v82, 0, v82, v83
	v_add_u32_e32 v83, 0x10400, v82
	v_cmp_eq_u32_e64 s[6:7], 0, v103
	s_waitcnt vmcnt(5)
	v_mfma_f32_32x32x16_bf16 v[2:17], v[86:89], v[62:65], v[2:17]
	v_mfma_f32_32x32x16_bf16 v[18:33], v[86:89], v[58:61], v[18:33]
	s_waitcnt vmcnt(4)
	v_mfma_f32_32x32x16_bf16 v[2:17], v[90:93], v[50:53], v[2:17]
	v_mfma_f32_32x32x16_bf16 v[18:33], v[90:93], v[54:57], v[18:33]
	s_waitcnt vmcnt(3)
	v_mfma_f32_32x32x16_bf16 v[2:17], v[94:97], v[66:69], v[2:17]
	v_mfma_f32_32x32x16_bf16 v[18:33], v[94:97], v[70:73], v[18:33]
	s_waitcnt vmcnt(2)
	v_mfma_f32_32x32x16_bf16 v[2:17], v[156:159], v[74:77], v[2:17]
	v_mfma_f32_32x32x16_bf16 v[18:33], v[156:159], v[78:81], v[18:33]
	s_waitcnt vmcnt(1) lgkmcnt(1)
	v_mfma_f32_32x32x16_bf16 v[2:17], v[160:163], v[34:37], v[2:17]
	s_waitcnt lgkmcnt(0)
	v_mfma_f32_32x32x16_bf16 v[18:33], v[160:163], v[38:41], v[18:33]
	ds_read_b128 v[34:37], v0 offset:224
	ds_read_b128 v[38:41], v0 offset:8896
	s_waitcnt vmcnt(0) lgkmcnt(1)
	v_mfma_f32_32x32x16_bf16 v[2:17], v[164:167], v[34:37], v[2:17]
	s_waitcnt lgkmcnt(0)
	v_mfma_f32_32x32x16_bf16 v[18:33], v[164:167], v[38:41], v[18:33]
	global_load_dwordx4 v[34:37], v[98:99], off offset:384
	global_load_dwordx4 v[38:41], v[98:99], off offset:416
	global_load_dwordx4 v[42:45], v[98:99], off offset:448
	global_load_dwordx4 v[46:49], v[98:99], off offset:480
	s_nop 5
	v_mov_b32_e32 v50, v2
	s_nop 0
	v_mov_b32_e32 v51, v18
	v_mov_b32_e32 v18, v3
	s_waitcnt vmcnt(3)
	v_pk_add_f32 v[2:3], v[18:19], v[34:35] op_sel:[0,1]
	s_nop 0
	v_cvt_pk_bf16_f32 v67, v2, v3
	v_mov_b32_e32 v2, v4
	v_mov_b32_e32 v3, v20
	v_pk_add_f32 v[2:3], v[2:3], v[36:37] op_sel_hi:[1,0]
	v_mov_b32_e32 v20, v5
	v_mov_b32_e32 v0, v37
	v_cvt_pk_bf16_f32 v68, v2, v3
	v_pk_add_f32 v[2:3], v[20:21], v[0:1] op_sel_hi:[1,0]
	s_waitcnt vmcnt(2)
	v_mov_b32_e32 v0, v41
	v_cvt_pk_bf16_f32 v69, v2, v3
	v_mov_b32_e32 v2, v6
	v_mov_b32_e32 v3, v22
	v_pk_add_f32 v[2:3], v[2:3], v[38:39] op_sel_hi:[1,0]
	v_mov_b32_e32 v22, v7
	v_cvt_pk_bf16_f32 v70, v2, v3
	v_pk_add_f32 v[2:3], v[22:23], v[38:39] op_sel:[0,1]
	v_pk_add_f32 v[50:51], v[50:51], v[34:35] op_sel_hi:[1,0]
	v_cvt_pk_bf16_f32 v71, v2, v3
	v_mov_b32_e32 v2, v8
	v_mov_b32_e32 v3, v24
	v_pk_add_f32 v[2:3], v[2:3], v[40:41] op_sel_hi:[1,0]
	v_mov_b32_e32 v24, v9
	v_cvt_pk_bf16_f32 v72, v2, v3
	v_pk_add_f32 v[2:3], v[24:25], v[0:1] op_sel_hi:[1,0]
	s_waitcnt vmcnt(1)
	v_mov_b32_e32 v0, v45
	v_cvt_pk_bf16_f32 v73, v2, v3
	v_mov_b32_e32 v2, v10
	v_mov_b32_e32 v3, v26
	v_pk_add_f32 v[2:3], v[2:3], v[42:43] op_sel_hi:[1,0]
	v_mov_b32_e32 v26, v11
	v_cvt_pk_bf16_f32 v74, v2, v3
	v_pk_add_f32 v[2:3], v[26:27], v[42:43] op_sel:[0,1]
	v_cvt_pk_bf16_f32 v66, v50, v51
	v_cvt_pk_bf16_f32 v75, v2, v3
	v_mov_b32_e32 v2, v12
	v_mov_b32_e32 v3, v28
	v_pk_add_f32 v[2:3], v[2:3], v[44:45] op_sel_hi:[1,0]
	v_mov_b32_e32 v28, v13
	v_cvt_pk_bf16_f32 v76, v2, v3
	v_pk_add_f32 v[2:3], v[28:29], v[0:1] op_sel_hi:[1,0]
	s_waitcnt vmcnt(0)
	v_mov_b32_e32 v0, v49
	v_cvt_pk_bf16_f32 v77, v2, v3
	v_mov_b32_e32 v2, v14
	v_mov_b32_e32 v3, v30
	v_pk_add_f32 v[2:3], v[2:3], v[46:47] op_sel_hi:[1,0]
	v_mov_b32_e32 v30, v15
	v_cvt_pk_bf16_f32 v78, v2, v3
	v_pk_add_f32 v[2:3], v[30:31], v[46:47] op_sel:[0,1]
	s_nop 0
	v_cvt_pk_bf16_f32 v79, v2, v3
	v_mov_b32_e32 v2, v16
	v_mov_b32_e32 v3, v32
	v_pk_add_f32 v[2:3], v[2:3], v[48:49] op_sel_hi:[1,0]
	v_mov_b32_e32 v32, v17
	v_cvt_pk_bf16_f32 v80, v2, v3
	v_pk_add_f32 v[2:3], v[32:33], v[0:1] op_sel_hi:[1,0]
	v_lshlrev_b32_e32 v0, 4, v103
	v_cvt_pk_bf16_f32 v81, v2, v3
	v_lshl_add_u64 v[2:3], s[14:15], 0, v[0:1]
	v_lshl_add_u64 v[2:3], v[2:3], 0, s[4:5]
	v_add_co_u32_e32 v4, vcc, s74, v2
	s_movk_i32 s4, 0x2000
	s_nop 0
	v_addc_co_u32_e32 v5, vcc, 0, v3, vcc
	v_add_co_u32_e32 v6, vcc, s4, v2
	global_load_dwordx4 v[62:65], v[2:3], off
	global_load_dwordx4 v[58:61], v[2:3], off offset:2048
	v_addc_co_u32_e32 v7, vcc, 0, v3, vcc
	s_movk_i32 s4, 0x3000
	global_load_dwordx4 v[54:57], v[6:7], off offset:-4096
	global_load_dwordx4 v[50:53], v[4:5], off offset:2048
	global_load_dwordx4 v[46:49], v[6:7], off
	global_load_dwordx4 v[42:45], v[6:7], off offset:2048
	v_add_co_u32_e32 v4, vcc, s4, v2
	s_movk_i32 s4, 0x4000
	s_nop 0
	v_addc_co_u32_e32 v5, vcc, 0, v3, vcc
	v_add_co_u32_e32 v6, vcc, s4, v2
	s_movk_i32 s4, 0x5000
	s_nop 0
	v_addc_co_u32_e32 v7, vcc, 0, v3, vcc
	global_load_dwordx4 v[38:41], v[6:7], off offset:-4096
	global_load_dwordx4 v[34:37], v[4:5], off offset:2048
	global_load_dwordx4 v[30:33], v[6:7], off
	global_load_dwordx4 v[26:29], v[6:7], off offset:2048
	v_add_co_u32_e32 v4, vcc, s4, v2
	s_movk_i32 s4, 0x6000
	s_nop 0
	v_addc_co_u32_e32 v5, vcc, 0, v3, vcc
	v_add_co_u32_e32 v6, vcc, s4, v2
	s_movk_i32 s4, 0x7000
	s_nop 0
	v_addc_co_u32_e32 v7, vcc, 0, v3, vcc
	v_add_co_u32_e32 v2, vcc, s4, v2
	global_load_dwordx4 v[22:25], v[6:7], off offset:-4096
	global_load_dwordx4 v[18:21], v[4:5], off offset:2048
	global_load_dwordx4 v[14:17], v[6:7], off
	global_load_dwordx4 v[10:13], v[6:7], off offset:2048
	v_addc_co_u32_e32 v3, vcc, 0, v3, vcc
	global_load_dwordx4 v[6:9], v[2:3], off
	s_nop 0
	global_load_dwordx4 v[2:5], v[2:3], off offset:2048
	s_barrier
	ds_write_b16 v82, v107
	ds_write_b16_d16_hi v82, v107 offset:64
	ds_write_b16 v82, v108 offset:1040
	ds_write_b16_d16_hi v82, v108 offset:1104
	ds_write_b16 v82, v109 offset:2080
	ds_write_b16_d16_hi v82, v109 offset:2144
	ds_write_b16 v82, v110 offset:3120
	ds_write_b16_d16_hi v82, v110 offset:3184
	ds_write_b16 v82, v111 offset:8320
	ds_write_b16_d16_hi v82, v111 offset:8384
	ds_write_b16 v82, v112 offset:9360
	ds_write_b16_d16_hi v82, v112 offset:9424
	ds_write_b16 v82, v113 offset:10400
	ds_write_b16_d16_hi v82, v113 offset:10464
	ds_write_b16 v82, v114 offset:11440
	ds_write_b16_d16_hi v82, v114 offset:11504
	ds_write_b16 v82, v115 offset:16640
	ds_write_b16_d16_hi v82, v115 offset:16704
	ds_write_b16 v82, v116 offset:17680
	ds_write_b16_d16_hi v82, v116 offset:17744
	ds_write_b16 v82, v117 offset:18720
	ds_write_b16_d16_hi v82, v117 offset:18784
	ds_write_b16 v82, v118 offset:19760
	ds_write_b16_d16_hi v82, v118 offset:19824
	ds_write_b16 v82, v119 offset:24960
	ds_write_b16_d16_hi v82, v119 offset:25024
	ds_write_b16 v82, v120 offset:26000
	ds_write_b16_d16_hi v82, v120 offset:26064
	ds_write_b16 v82, v121 offset:27040
	ds_write_b16_d16_hi v82, v121 offset:27104
	ds_write_b16 v82, v122 offset:28080
	ds_write_b16_d16_hi v82, v122 offset:28144
	ds_write_b16 v82, v123 offset:33280
	ds_write_b16_d16_hi v82, v123 offset:33344
	ds_write_b16 v82, v124 offset:34320
	ds_write_b16_d16_hi v82, v124 offset:34384
	ds_write_b16 v82, v125 offset:35360
	ds_write_b16_d16_hi v82, v125 offset:35424
	ds_write_b16 v82, v126 offset:36400
	ds_write_b16_d16_hi v82, v126 offset:36464
	ds_write_b16 v82, v127 offset:41600
	ds_write_b16_d16_hi v82, v127 offset:41664
	ds_write_b16 v82, v128 offset:42640
	ds_write_b16_d16_hi v82, v128 offset:42704
	ds_write_b16 v82, v129 offset:43680
	ds_write_b16_d16_hi v82, v129 offset:43744
	ds_write_b16 v82, v130 offset:44720
	ds_write_b16_d16_hi v82, v130 offset:44784
	ds_write_b16 v82, v131 offset:49920
	ds_write_b16_d16_hi v82, v131 offset:49984
	ds_write_b16 v82, v132 offset:50960
	ds_write_b16_d16_hi v82, v132 offset:51024
	ds_write_b16 v82, v133 offset:52000
	ds_write_b16_d16_hi v82, v133 offset:52064
	ds_write_b16 v82, v134 offset:53040
	ds_write_b16_d16_hi v82, v134 offset:53104
	ds_write_b16 v82, v135 offset:58240
	ds_write_b16_d16_hi v82, v135 offset:58304
	ds_write_b16 v82, v136 offset:59280
	ds_write_b16_d16_hi v82, v136 offset:59344
	ds_write_b16 v82, v137 offset:60320
	ds_write_b16_d16_hi v82, v137 offset:60384
	ds_write_b16 v82, v138 offset:61360
	ds_write_b16_d16_hi v82, v138 offset:61424
	ds_write_b16 v83, v154
	v_add_u32_e32 v83, 0x10440, v82
	ds_write_b16_d16_hi v83, v154
	v_add_u32_e32 v83, 0x10810, v82
	ds_write_b16 v83, v150
	v_add_u32_e32 v83, 0x10850, v82
	ds_write_b16_d16_hi v83, v150
	v_add_u32_e32 v83, 0x10c20, v82
	ds_write_b16 v83, v151
	v_add_u32_e32 v83, 0x10c60, v82
	ds_write_b16_d16_hi v83, v151
	v_add_u32_e32 v83, 0x11030, v82
	ds_write_b16 v83, v152
	v_add_u32_e32 v83, 0x11070, v82
	ds_write_b16_d16_hi v83, v152
	v_add_u32_e32 v83, 0x12480, v82
	ds_write_b16 v83, v153
	v_add_u32_e32 v83, 0x124c0, v82
	ds_write_b16_d16_hi v83, v153
	v_add_u32_e32 v83, 0x12890, v82
	ds_write_b16 v83, v146
	v_add_u32_e32 v83, 0x128d0, v82
	ds_write_b16_d16_hi v83, v146
	v_add_u32_e32 v83, 0x12ca0, v82
	ds_write_b16 v83, v147
	v_add_u32_e32 v83, 0x12ce0, v82
	ds_write_b16_d16_hi v83, v147
	v_add_u32_e32 v83, 0x130b0, v82
	ds_write_b16 v83, v148
	v_add_u32_e32 v83, 0x130f0, v82
	ds_write_b16_d16_hi v83, v148
	v_add_u32_e32 v83, 0x14500, v82
	ds_write_b16 v83, v149
	v_add_u32_e32 v83, 0x14540, v82
	ds_write_b16_d16_hi v83, v149
	v_add_u32_e32 v83, 0x14910, v82
	ds_write_b16 v83, v142
	v_add_u32_e32 v83, 0x14950, v82
	ds_write_b16_d16_hi v83, v142
	v_add_u32_e32 v83, 0x14d20, v82
	ds_write_b16 v83, v143
	v_add_u32_e32 v83, 0x14d60, v82
	ds_write_b16_d16_hi v83, v143
	v_add_u32_e32 v83, 0x15130, v82
	ds_write_b16 v83, v144
	v_add_u32_e32 v83, 0x15170, v82
	ds_write_b16_d16_hi v83, v144
	v_add_u32_e32 v83, 0x16580, v82
	ds_write_b16 v83, v145
	v_add_u32_e32 v83, 0x165c0, v82
	ds_write_b16_d16_hi v83, v145
	v_add_u32_e32 v83, 0x16990, v82
	ds_write_b16 v83, v139
	v_add_u32_e32 v83, 0x169d0, v82
	ds_write_b16_d16_hi v83, v139
	v_add_u32_e32 v83, 0x16da0, v82
	ds_write_b16 v83, v140
	v_add_u32_e32 v83, 0x16de0, v82
	ds_write_b16_d16_hi v83, v140
	v_add_u32_e32 v83, 0x171b0, v82
	ds_write_b16 v83, v141
	v_add_u32_e32 v83, 0x171f0, v82
	ds_write_b16_d16_hi v83, v141
	v_add_u32_e32 v83, 0x18600, v82
	ds_write_b16 v83, v66
	v_add_u32_e32 v83, 0x18640, v82
	ds_write_b16_d16_hi v83, v66
	v_add_u32_e32 v66, 0x18a10, v82
	ds_write_b16 v66, v67
	v_add_u32_e32 v66, 0x18a50, v82
	ds_write_b16_d16_hi v66, v67
	v_add_u32_e32 v66, 0x18e20, v82
	ds_write_b16 v66, v68
	v_add_u32_e32 v66, 0x18e60, v82
	ds_write_b16_d16_hi v66, v68
	v_add_u32_e32 v66, 0x19230, v82
	ds_write_b16 v66, v69
	v_add_u32_e32 v66, 0x19270, v82
	ds_write_b16_d16_hi v66, v69
	v_add_u32_e32 v66, 0x1a680, v82
	ds_write_b16 v66, v70
	v_add_u32_e32 v66, 0x1a6c0, v82
	ds_write_b16_d16_hi v66, v70
	v_add_u32_e32 v66, 0x1aa90, v82
	ds_write_b16 v66, v71
	v_add_u32_e32 v66, 0x1aad0, v82
	ds_write_b16_d16_hi v66, v71
	v_add_u32_e32 v66, 0x1aea0, v82
	ds_write_b16 v66, v72
	v_add_u32_e32 v66, 0x1aee0, v82
	ds_write_b16_d16_hi v66, v72
	v_add_u32_e32 v66, 0x1b2b0, v82
	ds_write_b16 v66, v73
	v_add_u32_e32 v66, 0x1b2f0, v82
	ds_write_b16_d16_hi v66, v73
	v_add_u32_e32 v66, 0x1c700, v82
	ds_write_b16 v66, v74
	v_add_u32_e32 v66, 0x1c740, v82
	ds_write_b16_d16_hi v66, v74
	v_add_u32_e32 v66, 0x1cb10, v82
	ds_write_b16 v66, v75
	v_add_u32_e32 v66, 0x1cb50, v82
	ds_write_b16_d16_hi v66, v75
	v_add_u32_e32 v66, 0x1cf20, v82
	ds_write_b16 v66, v76
	v_add_u32_e32 v66, 0x1cf60, v82
	ds_write_b16_d16_hi v66, v76
	v_add_u32_e32 v66, 0x1d330, v82
	ds_write_b16 v66, v77
	v_add_u32_e32 v66, 0x1d370, v82
	ds_write_b16_d16_hi v66, v77
	v_add_u32_e32 v66, 0x1e780, v82
	ds_write_b16 v66, v78
	v_add_u32_e32 v66, 0x1e7c0, v82
	ds_write_b16_d16_hi v66, v78
	v_add_u32_e32 v66, 0x1eb90, v82
	ds_write_b16 v66, v79
	v_add_u32_e32 v66, 0x1ebd0, v82
	ds_write_b16_d16_hi v66, v79
	v_add_u32_e32 v66, 0x1efa0, v82
	v_add_u32_e32 v70, 0, v0
	v_xor_b32_e32 v0, 8, v234
	ds_write_b16 v66, v80
	v_add_u32_e32 v66, 0x1efe0, v82
	v_cmp_lt_i32_e32 vcc, v0, v104
	ds_write_b16_d16_hi v66, v80
	v_add_u32_e32 v66, 0x1f3b0, v82
	v_cndmask_b32_e32 v0, v234, v0, vcc
	s_mul_i32 s4, s12, 0x4100
	ds_write_b16 v66, v81
	v_add_u32_e32 v66, 0x1f3f0, v82
	v_lshlrev_b32_e32 v68, 2, v0
	v_xor_b32_e32 v0, 16, v234
	v_add_u32_e32 v69, s4, v70
	ds_write_b16_d16_hi v66, v81
	s_waitcnt lgkmcnt(0)
	s_barrier
	v_cmp_lt_i32_e32 vcc, v0, v104
	ds_read_b128 v[74:77], v69
	ds_read_b128 v[82:85], v69 offset:1040
	v_cndmask_b32_e32 v0, v234, v0, vcc
	v_lshlrev_b32_e32 v67, 2, v0
	v_xor_b32_e32 v0, 32, v234
	v_cmp_lt_i32_e32 vcc, v0, v104
	s_waitcnt vmcnt(15)
	v_lshlrev_b32_e32 v71, 16, v62
	v_and_b32_e32 v62, 0xffff0000, v62
	v_cndmask_b32_e32 v0, v234, v0, vcc
	v_lshlrev_b32_e32 v66, 2, v0
	s_waitcnt lgkmcnt(1)
	v_lshlrev_b32_e32 v0, 16, v74
	v_mul_f32_e32 v71, v71, v0
	v_and_b32_e32 v0, 0xffff0000, v74
	v_mul_f32_e32 v72, v62, v0
	v_lshlrev_b32_e32 v0, 16, v75
	v_lshlrev_b32_e32 v62, 16, v63
	v_mul_f32_e32 v73, v62, v0
	v_and_b32_e32 v0, 0xffff0000, v75
	v_and_b32_e32 v62, 0xffff0000, v63
	v_mul_f32_e32 v74, v62, v0
	v_lshlrev_b32_e32 v0, 16, v76
	v_lshlrev_b32_e32 v62, 16, v64
	v_mul_f32_e32 v62, v62, v0
	v_and_b32_e32 v0, 0xffff0000, v76
	v_and_b32_e32 v63, 0xffff0000, v64
	v_mul_f32_e32 v63, v63, v0
	v_lshlrev_b32_e32 v0, 16, v77
	v_lshlrev_b32_e32 v64, 16, v65
	v_mul_f32_e32 v64, v64, v0
	v_and_b32_e32 v0, 0xffff0000, v77
	v_and_b32_e32 v65, 0xffff0000, v65
	v_mul_f32_e32 v65, v65, v0
	s_waitcnt lgkmcnt(0)
	v_lshlrev_b32_e32 v0, 16, v82
	s_waitcnt vmcnt(14)
	v_lshlrev_b32_e32 v75, 16, v58
	v_mul_f32_e32 v79, v75, v0
	v_and_b32_e32 v0, 0xffff0000, v82
	v_and_b32_e32 v58, 0xffff0000, v58
	v_mul_f32_e32 v80, v58, v0
	v_lshlrev_b32_e32 v0, 16, v83
	v_lshlrev_b32_e32 v58, 16, v59
	v_mul_f32_e32 v81, v58, v0
	v_and_b32_e32 v0, 0xffff0000, v83
	v_and_b32_e32 v58, 0xffff0000, v59
	v_mul_f32_e32 v82, v58, v0
	v_lshlrev_b32_e32 v0, 16, v84
	v_lshlrev_b32_e32 v58, 16, v60
	v_mul_f32_e32 v75, v58, v0
	v_and_b32_e32 v0, 0xffff0000, v84
	v_and_b32_e32 v58, 0xffff0000, v60
	v_mul_f32_e32 v76, v58, v0
	v_lshlrev_b32_e32 v0, 16, v85
	v_lshlrev_b32_e32 v58, 16, v61
	v_mul_f32_e32 v77, v58, v0
	v_and_b32_e32 v0, 0xffff0000, v85
	ds_read_b128 v[84:87], v69 offset:2080
	ds_read_b128 v[90:93], v69 offset:3120
	v_and_b32_e32 v58, 0xffff0000, v61
	v_mul_f32_e32 v78, v58, v0
	s_waitcnt vmcnt(13)
	v_lshlrev_b32_e32 v58, 16, v54
	s_waitcnt lgkmcnt(1)
	v_lshlrev_b32_e32 v0, 16, v84
	v_mul_f32_e32 v58, v58, v0
	v_and_b32_e32 v0, 0xffff0000, v84
	v_and_b32_e32 v54, 0xffff0000, v54
	v_mul_f32_e32 v59, v54, v0
	v_lshlrev_b32_e32 v0, 16, v85
	v_lshlrev_b32_e32 v54, 16, v55
	v_mul_f32_e32 v60, v54, v0
	v_and_b32_e32 v0, 0xffff0000, v85
	v_and_b32_e32 v54, 0xffff0000, v55
	v_mul_f32_e32 v61, v54, v0
	v_lshlrev_b32_e32 v0, 16, v86
	v_lshlrev_b32_e32 v54, 16, v56
	v_mul_f32_e32 v54, v54, v0
	v_and_b32_e32 v0, 0xffff0000, v86
	v_and_b32_e32 v55, 0xffff0000, v56
	v_mul_f32_e32 v55, v55, v0
	v_lshlrev_b32_e32 v0, 16, v87
	v_lshlrev_b32_e32 v56, 16, v57
	v_mul_f32_e32 v56, v56, v0
	v_and_b32_e32 v0, 0xffff0000, v87
	v_and_b32_e32 v57, 0xffff0000, v57
	v_mul_f32_e32 v57, v57, v0
	s_waitcnt lgkmcnt(0)
	v_lshlrev_b32_e32 v0, 16, v90
	s_waitcnt vmcnt(12)
	v_lshlrev_b32_e32 v83, 16, v50
	v_mul_f32_e32 v87, v83, v0
	v_and_b32_e32 v0, 0xffff0000, v90
	v_and_b32_e32 v50, 0xffff0000, v50
	v_mul_f32_e32 v88, v50, v0
	v_lshlrev_b32_e32 v0, 16, v91
	v_lshlrev_b32_e32 v50, 16, v51
	v_mul_f32_e32 v89, v50, v0
	v_and_b32_e32 v0, 0xffff0000, v91
	v_and_b32_e32 v50, 0xffff0000, v51
	v_mul_f32_e32 v90, v50, v0
	v_lshlrev_b32_e32 v0, 16, v92
	v_lshlrev_b32_e32 v50, 16, v52
	v_mul_f32_e32 v83, v50, v0
	v_and_b32_e32 v0, 0xffff0000, v92
	v_and_b32_e32 v50, 0xffff0000, v52
	v_mul_f32_e32 v84, v50, v0
	v_lshlrev_b32_e32 v0, 16, v93
	v_lshlrev_b32_e32 v50, 16, v53
	v_mul_f32_e32 v85, v50, v0
	v_and_b32_e32 v0, 0xffff0000, v93
	ds_read_b128 v[92:95], v69 offset:4160
	ds_read_b128 v[104:107], v69 offset:5200
	v_and_b32_e32 v50, 0xffff0000, v53
	v_mul_f32_e32 v86, v50, v0
	s_waitcnt vmcnt(11)
	v_lshlrev_b32_e32 v50, 16, v46
	s_waitcnt lgkmcnt(1)
	v_lshlrev_b32_e32 v0, 16, v92
	v_mul_f32_e32 v50, v50, v0
	v_and_b32_e32 v0, 0xffff0000, v92
	v_and_b32_e32 v46, 0xffff0000, v46
	v_mul_f32_e32 v51, v46, v0
	v_lshlrev_b32_e32 v0, 16, v93
	v_lshlrev_b32_e32 v46, 16, v47
	v_mul_f32_e32 v52, v46, v0
	v_and_b32_e32 v0, 0xffff0000, v93
	v_and_b32_e32 v46, 0xffff0000, v47
	v_mul_f32_e32 v53, v46, v0
	v_lshlrev_b32_e32 v0, 16, v94
	v_lshlrev_b32_e32 v46, 16, v48
	v_mul_f32_e32 v46, v46, v0
	v_and_b32_e32 v0, 0xffff0000, v94
	v_and_b32_e32 v47, 0xffff0000, v48
	v_mul_f32_e32 v47, v47, v0
	v_lshlrev_b32_e32 v0, 16, v95
	v_lshlrev_b32_e32 v48, 16, v49
	v_mul_f32_e32 v48, v48, v0
	v_and_b32_e32 v0, 0xffff0000, v95
	v_and_b32_e32 v49, 0xffff0000, v49
	v_mul_f32_e32 v49, v49, v0
	s_waitcnt lgkmcnt(0)
	v_lshlrev_b32_e32 v0, 16, v104
	s_waitcnt vmcnt(10)
	v_lshlrev_b32_e32 v91, 16, v42
	v_mul_f32_e32 v95, v91, v0
	v_and_b32_e32 v0, 0xffff0000, v104
	v_and_b32_e32 v42, 0xffff0000, v42
	v_mul_f32_e32 v96, v42, v0
	v_lshlrev_b32_e32 v0, 16, v105
	v_lshlrev_b32_e32 v42, 16, v43
	v_mul_f32_e32 v97, v42, v0
	v_and_b32_e32 v0, 0xffff0000, v105
	v_and_b32_e32 v42, 0xffff0000, v43
	v_mul_f32_e32 v98, v42, v0
	v_lshlrev_b32_e32 v0, 16, v106
	v_lshlrev_b32_e32 v42, 16, v44
	v_mul_f32_e32 v91, v42, v0
	v_and_b32_e32 v0, 0xffff0000, v106
	v_and_b32_e32 v42, 0xffff0000, v44
	v_mul_f32_e32 v92, v42, v0
	v_lshlrev_b32_e32 v0, 16, v107
	v_lshlrev_b32_e32 v42, 16, v45
	v_mul_f32_e32 v93, v42, v0
	v_and_b32_e32 v0, 0xffff0000, v107
	ds_read_b128 v[104:107], v69 offset:6240
	ds_read_b128 v[108:111], v69 offset:7280
	v_and_b32_e32 v42, 0xffff0000, v45
	v_mul_f32_e32 v94, v42, v0
	s_waitcnt vmcnt(9)
	v_lshlrev_b32_e32 v42, 16, v38
	s_waitcnt lgkmcnt(1)
	v_lshlrev_b32_e32 v0, 16, v104
	v_mul_f32_e32 v42, v42, v0
	v_and_b32_e32 v0, 0xffff0000, v104
	v_and_b32_e32 v38, 0xffff0000, v38
	v_mul_f32_e32 v43, v38, v0
	v_lshlrev_b32_e32 v0, 16, v105
	v_lshlrev_b32_e32 v38, 16, v39
	v_mul_f32_e32 v44, v38, v0
	v_and_b32_e32 v0, 0xffff0000, v105
	v_and_b32_e32 v38, 0xffff0000, v39
	v_mul_f32_e32 v45, v38, v0
	v_lshlrev_b32_e32 v0, 16, v106
	v_lshlrev_b32_e32 v38, 16, v40
	v_mul_f32_e32 v38, v38, v0
	v_and_b32_e32 v0, 0xffff0000, v106
	v_and_b32_e32 v39, 0xffff0000, v40
	v_mul_f32_e32 v39, v39, v0
	v_lshlrev_b32_e32 v0, 16, v107
	v_lshlrev_b32_e32 v40, 16, v41
	v_mul_f32_e32 v40, v40, v0
	v_and_b32_e32 v0, 0xffff0000, v107
	v_and_b32_e32 v41, 0xffff0000, v41
	v_mul_f32_e32 v41, v41, v0
	s_waitcnt lgkmcnt(0)
	v_lshlrev_b32_e32 v0, 16, v108
	s_waitcnt vmcnt(8)
	v_lshlrev_b32_e32 v99, 16, v34
	v_mul_f32_e32 v105, v99, v0
	v_and_b32_e32 v0, 0xffff0000, v108
	v_and_b32_e32 v34, 0xffff0000, v34
	v_mul_f32_e32 v106, v34, v0
	v_lshlrev_b32_e32 v0, 16, v109
	v_lshlrev_b32_e32 v34, 16, v35
	v_mul_f32_e32 v107, v34, v0
	v_and_b32_e32 v0, 0xffff0000, v109
	v_and_b32_e32 v34, 0xffff0000, v35
	v_mul_f32_e32 v108, v34, v0
	v_lshlrev_b32_e32 v0, 16, v110
	v_lshlrev_b32_e32 v34, 16, v36
	v_mul_f32_e32 v99, v34, v0
	v_and_b32_e32 v0, 0xffff0000, v110
	v_and_b32_e32 v34, 0xffff0000, v36
	v_mul_f32_e32 v36, v34, v0
	v_lshlrev_b32_e32 v0, 16, v111
	v_lshlrev_b32_e32 v34, 16, v37
	v_mul_f32_e32 v104, v34, v0
	v_and_b32_e32 v0, 0xffff0000, v111
	v_and_b32_e32 v34, 0xffff0000, v37
	v_mul_f32_e32 v37, v34, v0
	v_max3_f32 v0, |v71|, 0, |v72|
	v_max3_f32 v0, v0, |v73|, |v74|
	v_max3_f32 v0, v0, |v62|, |v63|
	v_max3_f32 v0, v0, |v64|, |v65|
	s_nop 1
	v_max_f32_dpp v0, v0, v0 quad_perm:[1,0,3,2] row_mask:0xf bank_mask:0xf
	s_nop 1
	v_max_f32_dpp v0, v0, v0 quad_perm:[2,3,0,1] row_mask:0xf bank_mask:0xf
	s_nop 1
	v_max_f32_dpp v0, v0, v0 row_half_mirror row_mask:0xf bank_mask:0xf
	s_nop 1
	v_max_f32_dpp v0, v0, v0 row_ror:8 row_mask:0xf bank_mask:0xf
	v_mov_b32_e32 v114, v0
	s_nop 1
	v_permlane16_swap_b32_e32 v0, v114
	s_nop 0
	v_max_f32_e32 v0, v0, v114
	v_mov_b32_e32 v114, v0
	s_nop 1
	v_permlane32_swap_b32_e32 v0, v114
	s_nop 0
	v_max_f32_e32 v0, v0, v114
	v_mov_b32_e32 v114, v0
	v_max3_f32 v34, |v79|, 0, |v80|
	v_max3_f32 v34, v34, |v81|, |v82|
	v_max3_f32 v34, v34, |v75|, |v76|
	v_max3_f32 v34, v34, |v77|, |v78|
	s_waitcnt lgkmcnt(0)
	v_max_f32_e32 v114, v114, v114
	v_max_f32_e32 v0, v0, v114
	s_nop 1
	v_max_f32_dpp v34, v34, v34 quad_perm:[1,0,3,2] row_mask:0xf bank_mask:0xf
	s_nop 1
	v_max_f32_dpp v34, v34, v34 quad_perm:[2,3,0,1] row_mask:0xf bank_mask:0xf
	s_nop 1
	v_max_f32_dpp v34, v34, v34 row_half_mirror row_mask:0xf bank_mask:0xf
	s_nop 1
	v_max_f32_dpp v34, v34, v34 row_ror:8 row_mask:0xf bank_mask:0xf
	v_mov_b32_e32 v114, v34
	s_nop 1
	v_permlane16_swap_b32_e32 v34, v114
	s_nop 0
	v_max_f32_e32 v34, v34, v114
	v_mov_b32_e32 v114, v34
	s_nop 1
	v_permlane32_swap_b32_e32 v34, v114
	s_nop 0
	v_max_f32_e32 v34, v34, v114
	v_mov_b32_e32 v114, v34
	v_max3_f32 v35, |v58|, 0, |v59|
	v_max3_f32 v35, v35, |v60|, |v61|
	v_max3_f32 v35, v35, |v54|, |v55|
	v_max3_f32 v35, v35, |v56|, |v57|
	s_waitcnt lgkmcnt(0)
	v_max_f32_e32 v114, v114, v114
	v_max_f32_e32 v34, v34, v114
	s_nop 1
	v_max_f32_dpp v35, v35, v35 quad_perm:[1,0,3,2] row_mask:0xf bank_mask:0xf
	s_nop 1
	v_max_f32_dpp v35, v35, v35 quad_perm:[2,3,0,1] row_mask:0xf bank_mask:0xf
	s_nop 1
	v_max_f32_dpp v35, v35, v35 row_half_mirror row_mask:0xf bank_mask:0xf
	s_nop 1
	v_max_f32_dpp v35, v35, v35 row_ror:8 row_mask:0xf bank_mask:0xf
	v_mov_b32_e32 v114, v35
	s_nop 1
	v_permlane16_swap_b32_e32 v35, v114
	s_nop 0
	v_max_f32_e32 v35, v35, v114
	v_mov_b32_e32 v114, v35
	s_nop 1
	v_permlane32_swap_b32_e32 v35, v114
	s_nop 0
	v_max_f32_e32 v35, v35, v114
	v_mov_b32_e32 v114, v35
	v_max3_f32 v109, |v87|, 0, |v88|
	v_max3_f32 v109, v109, |v89|, |v90|
	v_max3_f32 v109, v109, |v83|, |v84|
	v_max3_f32 v109, v109, |v85|, |v86|
	s_waitcnt lgkmcnt(0)
	v_max_f32_e32 v114, v114, v114
	v_max_f32_e32 v35, v35, v114
	s_nop 1
	v_max_f32_dpp v109, v109, v109 quad_perm:[1,0,3,2] row_mask:0xf bank_mask:0xf
	s_nop 1
	v_max_f32_dpp v109, v109, v109 quad_perm:[2,3,0,1] row_mask:0xf bank_mask:0xf
	s_nop 1
	v_max_f32_dpp v109, v109, v109 row_half_mirror row_mask:0xf bank_mask:0xf
	s_nop 1
	v_max_f32_dpp v109, v109, v109 row_ror:8 row_mask:0xf bank_mask:0xf
	v_mov_b32_e32 v114, v109
	s_nop 1
	v_permlane16_swap_b32_e32 v109, v114
	s_nop 0
	v_max_f32_e32 v109, v109, v114
	v_mov_b32_e32 v114, v109
	s_nop 1
	v_permlane32_swap_b32_e32 v109, v114
	s_nop 0
	v_max_f32_e32 v109, v109, v114
	v_mov_b32_e32 v114, v109
	v_max3_f32 v110, |v50|, 0, |v51|
	v_max3_f32 v110, v110, |v52|, |v53|
	v_max3_f32 v110, v110, |v46|, |v47|
	v_max3_f32 v110, v110, |v48|, |v49|
	s_waitcnt lgkmcnt(0)
	v_max_f32_e32 v114, v114, v114
	v_max_f32_e32 v109, v109, v114
	s_nop 1
	v_max_f32_dpp v110, v110, v110 quad_perm:[1,0,3,2] row_mask:0xf bank_mask:0xf
	s_nop 1
	v_max_f32_dpp v110, v110, v110 quad_perm:[2,3,0,1] row_mask:0xf bank_mask:0xf
	s_nop 1
	v_max_f32_dpp v110, v110, v110 row_half_mirror row_mask:0xf bank_mask:0xf
	s_nop 1
	v_max_f32_dpp v110, v110, v110 row_ror:8 row_mask:0xf bank_mask:0xf
	v_mov_b32_e32 v114, v110
	s_nop 1
	v_permlane16_swap_b32_e32 v110, v114
	s_nop 0
	v_max_f32_e32 v110, v110, v114
	v_mov_b32_e32 v114, v110
	s_nop 1
	v_permlane32_swap_b32_e32 v110, v114
	s_nop 0
	v_max_f32_e32 v110, v110, v114
	v_mov_b32_e32 v114, v110
	v_max3_f32 v111, |v95|, 0, |v96|
	v_max3_f32 v111, v111, |v97|, |v98|
	v_max3_f32 v111, v111, |v91|, |v92|
	v_max3_f32 v111, v111, |v93|, |v94|
	s_waitcnt lgkmcnt(0)
	v_max_f32_e32 v114, v114, v114
	v_max_f32_e32 v110, v110, v114
	s_nop 1
	v_max_f32_dpp v111, v111, v111 quad_perm:[1,0,3,2] row_mask:0xf bank_mask:0xf
	s_nop 1
	v_max_f32_dpp v111, v111, v111 quad_perm:[2,3,0,1] row_mask:0xf bank_mask:0xf
	s_nop 1
	v_max_f32_dpp v111, v111, v111 row_half_mirror row_mask:0xf bank_mask:0xf
	s_nop 1
	v_max_f32_dpp v111, v111, v111 row_ror:8 row_mask:0xf bank_mask:0xf
	v_mov_b32_e32 v114, v111
	s_nop 1
	v_permlane16_swap_b32_e32 v111, v114
	s_nop 0
	v_max_f32_e32 v111, v111, v114
	v_mov_b32_e32 v114, v111
	s_nop 1
	v_permlane32_swap_b32_e32 v111, v114
	s_nop 0
	v_max_f32_e32 v111, v111, v114
	v_mov_b32_e32 v114, v111
	v_max3_f32 v112, |v42|, 0, |v43|
	v_max3_f32 v112, v112, |v44|, |v45|
	v_max3_f32 v112, v112, |v38|, |v39|
	v_max3_f32 v112, v112, |v40|, |v41|
	s_waitcnt lgkmcnt(0)
	v_max_f32_e32 v114, v114, v114
	v_max_f32_e32 v111, v111, v114
	s_nop 1
	v_max_f32_dpp v112, v112, v112 quad_perm:[1,0,3,2] row_mask:0xf bank_mask:0xf
	s_nop 1
	v_max_f32_dpp v112, v112, v112 quad_perm:[2,3,0,1] row_mask:0xf bank_mask:0xf
	s_nop 1
	v_max_f32_dpp v112, v112, v112 row_half_mirror row_mask:0xf bank_mask:0xf
	s_nop 1
	v_max_f32_dpp v112, v112, v112 row_ror:8 row_mask:0xf bank_mask:0xf
	v_mov_b32_e32 v114, v112
	s_nop 1
	v_permlane16_swap_b32_e32 v112, v114
	s_nop 0
	v_max_f32_e32 v112, v112, v114
	v_mov_b32_e32 v114, v112
	s_nop 1
	v_permlane32_swap_b32_e32 v112, v114
	s_nop 0
	v_max_f32_e32 v112, v112, v114
	v_mov_b32_e32 v114, v112
	v_max3_f32 v113, |v105|, 0, |v106|
	v_max3_f32 v113, v113, |v107|, |v108|
	v_max3_f32 v113, v113, |v99|, |v36|
	v_max3_f32 v113, v113, |v104|, |v37|
	s_waitcnt lgkmcnt(0)
	v_max_f32_e32 v114, v114, v114
	v_max_f32_e32 v112, v112, v114
	s_nop 1
	v_max_f32_dpp v113, v113, v113 quad_perm:[1,0,3,2] row_mask:0xf bank_mask:0xf
	s_nop 1
	v_max_f32_dpp v113, v113, v113 quad_perm:[2,3,0,1] row_mask:0xf bank_mask:0xf
	s_nop 1
	v_max_f32_dpp v113, v113, v113 row_half_mirror row_mask:0xf bank_mask:0xf
	s_nop 1
	v_max_f32_dpp v113, v113, v113 row_ror:8 row_mask:0xf bank_mask:0xf
	v_mov_b32_e32 v114, v113
	s_nop 1
	v_permlane16_swap_b32_e32 v113, v114
	s_nop 0
	v_max_f32_e32 v113, v113, v114
	v_mov_b32_e32 v114, v113
	s_nop 1
	v_permlane32_swap_b32_e32 v113, v114
	s_nop 0
	v_max_f32_e32 v113, v113, v114
	v_mov_b32_e32 v114, v113
	s_waitcnt lgkmcnt(0)
	v_max_f32_e32 v114, v114, v114
	v_max_f32_e32 v113, v113, v114
	v_mov_b32_e32 v114, v0
	s_waitcnt lgkmcnt(0)
	v_max_f32_e32 v114, v114, v114
	v_max_f32_e32 v0, v0, v114
	v_mov_b32_e32 v114, v34
	s_waitcnt lgkmcnt(0)
	v_max_f32_e32 v114, v114, v114
	v_max_f32_e32 v34, v34, v114
	v_mov_b32_e32 v114, v35
	s_waitcnt lgkmcnt(0)
	v_max_f32_e32 v114, v114, v114
	v_max_f32_e32 v35, v35, v114
	v_mov_b32_e32 v114, v109
	s_waitcnt lgkmcnt(0)
	v_max_f32_e32 v114, v114, v114
	v_max_f32_e32 v109, v109, v114
	v_mov_b32_e32 v114, v110
	s_waitcnt lgkmcnt(0)
	v_max_f32_e32 v114, v114, v114
	v_max_f32_e32 v110, v110, v114
	v_mov_b32_e32 v114, v111
	s_waitcnt lgkmcnt(0)
	v_max_f32_e32 v114, v114, v114
	v_max_f32_e32 v111, v111, v114
	v_mov_b32_e32 v114, v112
	s_waitcnt lgkmcnt(0)
	v_max_f32_e32 v114, v114, v114
	v_max_f32_e32 v112, v112, v114
	v_mov_b32_e32 v114, v113
	s_waitcnt lgkmcnt(0)
	v_max_f32_e32 v114, v114, v114
	v_max_f32_e32 v113, v113, v114
	v_mov_b32_e32 v114, v0
	s_waitcnt lgkmcnt(0)
	v_max_f32_e32 v114, v114, v114
	v_max_f32_e32 v0, v0, v114
	v_mov_b32_e32 v114, v34
	s_waitcnt lgkmcnt(0)
	v_max_f32_e32 v114, v114, v114
	v_max_f32_e32 v34, v34, v114
	v_mov_b32_e32 v114, v35
	s_waitcnt lgkmcnt(0)
	v_max_f32_e32 v114, v114, v114
	v_max_f32_e32 v35, v35, v114
	v_mov_b32_e32 v114, v109
	s_waitcnt lgkmcnt(0)
	v_max_f32_e32 v114, v114, v114
	v_max_f32_e32 v109, v109, v114
	v_mov_b32_e32 v114, v110
	s_waitcnt lgkmcnt(0)
	v_max_f32_e32 v114, v114, v114
	v_max_f32_e32 v110, v110, v114
	v_mov_b32_e32 v114, v111
	s_waitcnt lgkmcnt(0)
	v_max_f32_e32 v114, v114, v114
	v_max_f32_e32 v111, v111, v114
	v_mov_b32_e32 v114, v112
	s_waitcnt lgkmcnt(0)
	v_max_f32_e32 v114, v114, v114
	v_max_f32_e32 v112, v112, v114
	v_mov_b32_e32 v114, v113
	s_waitcnt lgkmcnt(0)
	v_max_f32_e32 v114, v114, v114
	v_max_f32_e32 v113, v113, v114
	v_mov_b32_e32 v114, v0
	s_waitcnt lgkmcnt(0)
	v_max_f32_e32 v114, v114, v114
	v_max_f32_e32 v0, v0, v114
	v_mov_b32_e32 v114, v34
	s_waitcnt lgkmcnt(0)
	v_max_f32_e32 v114, v114, v114
	v_max_f32_e32 v34, v34, v114
	v_mov_b32_e32 v114, v35
	s_waitcnt lgkmcnt(0)
	v_max_f32_e32 v114, v114, v114
	v_max_f32_e32 v35, v35, v114
	v_mov_b32_e32 v114, v109
	s_waitcnt lgkmcnt(0)
	v_max_f32_e32 v114, v114, v114
	v_max_f32_e32 v109, v109, v114
	v_mov_b32_e32 v114, v110
	s_waitcnt lgkmcnt(0)
	v_max_f32_e32 v114, v114, v114
	v_max_f32_e32 v110, v110, v114
	v_mov_b32_e32 v114, v111
	s_waitcnt lgkmcnt(0)
	v_max_f32_e32 v114, v114, v114
	v_max_f32_e32 v111, v111, v114
	v_mov_b32_e32 v114, v112
	s_waitcnt lgkmcnt(0)
	v_max_f32_e32 v114, v114, v114
	v_max_f32_e32 v112, v112, v114
	v_mov_b32_e32 v114, v113
	s_waitcnt lgkmcnt(0)
	v_max_f32_e32 v114, v114, v114
	v_max_f32_e32 v114, v113, v114
	v_mov_b32_e32 v113, v0
	s_waitcnt lgkmcnt(0)
	v_max_f32_e32 v113, v113, v113
	v_max_f32_e32 v0, v0, v113
	v_mov_b32_e32 v113, v34
	s_waitcnt lgkmcnt(0)
	v_max_f32_e32 v113, v113, v113
	v_max_f32_e32 v120, v34, v113
	v_mov_b32_e32 v34, v35
	v_mov_b32_e32 v122, v120
	s_waitcnt lgkmcnt(0)
	v_max_f32_e32 v34, v34, v34
	v_max_f32_e32 v118, v35, v34
	v_mov_b32_e32 v34, v109
	v_mov_b32_e32 v121, v118
	s_waitcnt lgkmcnt(0)
	v_max_f32_e32 v34, v34, v34
	v_max_f32_e32 v116, v109, v34
	v_mov_b32_e32 v34, v110
	v_mov_b32_e32 v119, v116
	s_waitcnt lgkmcnt(0)
	v_max_f32_e32 v34, v34, v34
	v_max_f32_e32 v115, v110, v34
	v_mov_b32_e32 v34, v111
	v_mov_b32_e32 v117, v115
	s_waitcnt lgkmcnt(0)
	v_max_f32_e32 v34, v34, v34
	v_max_f32_e32 v113, v111, v34
	v_mov_b32_e32 v34, v112
	s_waitcnt lgkmcnt(0)
	v_max_f32_e32 v34, v34, v34
	v_max_f32_e32 v111, v112, v34
	v_mov_b32_e32 v34, v114
	v_mov_b32_e32 v112, v111
	s_waitcnt lgkmcnt(0)
	v_max_f32_e32 v34, v34, v34
	v_max_f32_e32 v109, v114, v34
	v_mov_b32_e32 v34, v0
	v_mov_b32_e32 v114, v113
	v_mov_b32_e32 v110, v109
	s_waitcnt lgkmcnt(0)
	v_max3_f32 v123, v0, v34, s72
	s_and_saveexec_b64 s[12:13], s[6:7]
	s_cbranch_execz .LBB0_490
	s_lshl_b64 s[4:5], s[16:17], 2
	s_add_u32 s4, s18, s4
	s_addc_u32 s5, s19, s5
	v_mul_f32_e32 v0, 0x3c010204, v123
	global_store_dword v1, v0, s[4:5]
